# conversion loops: redundant zero-initialisation of packed fp8 destinations removed
# speedup vs baseline: 1.0024x; 1.0024x over previous
; #define LAS __attribute__((address_space(3)))
; __device__ __forceinline__ float clamp448(float x) { return fminf(fmaxf(x, -448.f), 448.f); }
; __device__ __forceinline__ unsigned pk_fp8x4(float a, float b, float c, float d) {
;     int p = 0; p = __builtin_amdgcn_cvt_pk_fp8_f32(clamp448(a), clamp448(b), p, false); p = __builtin_amdgcn_cvt_pk_fp8_f32(clamp448(c), clamp448(d), p, true); return (unsigned)p; }
; __device__ __forceinline__ void conv8b_run(const Ctx& X, int first, int step, int count) {
;     ...
;         for (int q = 0; q < 4; ++q) { u32x4 o;
;             o.x = pk_fp8x4(v[0][q] * W8_SCALE, v[1][q] * W8_SCALE, v[2][q] * W8_SCALE, v[3][q] * W8_SCALE); o.y = pk_fp8x4(v[4][q] * W8_SCALE, v[5][q] * W8_SCALE, v[6][q] * W8_SCALE, v[7][q] * W8_SCALE);
;             o.z = pk_fp8x4(v[8][q] * W8_SCALE, v[9][q] * W8_SCALE, v[10][q] * W8_SCALE, v[11][q] * W8_SCALE); o.w = pk_fp8x4(v[12][q] * W8_SCALE, v[13][q] * W8_SCALE, v[14][q] * W8_SCALE, v[15][q] * W8_SCALE);
;             *(LAS u32x4*)(buf + (4 * X.lane + q) * CVT_STRIDE + 16 * X.wave) = o; }
.LBB0_141:
	s_waitcnt vmcnt(4)
	v_mul_f32_e32 v83, 0x42800000, v2
	v_mul_f32_e32 v84, 0x42800000, v14
	v_med3_f32 v83, v83, s21, v82
	v_med3_f32 v86, v84, s21, v82

; #define LAS __attribute__((address_space(3)))
; __device__ __forceinline__ float clamp448(float x) { return fminf(fmaxf(x, -448.f), 448.f); }
; __device__ __forceinline__ unsigned pk_fp8x4(float a, float b, float c, float d) {
;     int p = 0; p = __builtin_amdgcn_cvt_pk_fp8_f32(clamp448(a), clamp448(b), p, false); p = __builtin_amdgcn_cvt_pk_fp8_f32(clamp448(c), clamp448(d), p, true); return (unsigned)p; }
; __device__ __forceinline__ void conv8b_run(const Ctx& X, int first, int step, int count) {
;     ...
;         for (int q = 0; q < 4; ++q) { u32x4 o;
;             o.x = pk_fp8x4(v[0][q] * W8_SCALE, v[1][q] * W8_SCALE, v[2][q] * W8_SCALE, v[3][q] * W8_SCALE); o.y = pk_fp8x4(v[4][q] * W8_SCALE, v[5][q] * W8_SCALE, v[6][q] * W8_SCALE, v[7][q] * W8_SCALE);
;             o.z = pk_fp8x4(v[8][q] * W8_SCALE, v[9][q] * W8_SCALE, v[10][q] * W8_SCALE, v[11][q] * W8_SCALE); o.w = pk_fp8x4(v[12][q] * W8_SCALE, v[13][q] * W8_SCALE, v[14][q] * W8_SCALE, v[15][q] * W8_SCALE);
;             *(LAS u32x4*)(buf + (4 * X.lane + q) * CVT_STRIDE + 16 * X.wave) = o; }
	v_cvt_pk_fp8_f32 v84, v83, v86
	v_mul_f32_e32 v85, 0x42800000, v6
	v_mul_f32_e32 v83, 0x42800000, v30
	v_med3_f32 v85, v85, s21, v82
	v_med3_f32 v83, v83, s21, v82
	v_cvt_pk_fp8_f32 v84, v85, v83 op_sel:[0,0,1]
	v_mul_f32_e32 v83, 0x42800000, v22
	v_mul_f32_e32 v85, 0x42800000, v46
	v_med3_f32 v83, v83, s21, v82
	v_med3_f32 v87, v85, s21, v82

; #define LAS __attribute__((address_space(3)))
; __device__ __forceinline__ float clamp448(float x) { return fminf(fmaxf(x, -448.f), 448.f); }
; __device__ __forceinline__ unsigned pk_fp8x4(float a, float b, float c, float d) {
;     int p = 0; p = __builtin_amdgcn_cvt_pk_fp8_f32(clamp448(a), clamp448(b), p, false); p = __builtin_amdgcn_cvt_pk_fp8_f32(clamp448(c), clamp448(d), p, true); return (unsigned)p; }
; __device__ __forceinline__ void conv8b_run(const Ctx& X, int first, int step, int count) {
;     ...
;         for (int q = 0; q < 4; ++q) { u32x4 o;
;             o.x = pk_fp8x4(v[0][q] * W8_SCALE, v[1][q] * W8_SCALE, v[2][q] * W8_SCALE, v[3][q] * W8_SCALE); o.y = pk_fp8x4(v[4][q] * W8_SCALE, v[5][q] * W8_SCALE, v[6][q] * W8_SCALE, v[7][q] * W8_SCALE);
;             o.z = pk_fp8x4(v[8][q] * W8_SCALE, v[9][q] * W8_SCALE, v[10][q] * W8_SCALE, v[11][q] * W8_SCALE); o.w = pk_fp8x4(v[12][q] * W8_SCALE, v[13][q] * W8_SCALE, v[14][q] * W8_SCALE, v[15][q] * W8_SCALE);
;             *(LAS u32x4*)(buf + (4 * X.lane + q) * CVT_STRIDE + 16 * X.wave) = o; }
	v_cvt_pk_fp8_f32 v85, v83, v87
	v_mul_f32_e32 v86, 0x42800000, v38
	v_mul_f32_e32 v83, 0x42800000, v50
	v_med3_f32 v86, v86, s21, v82
	v_med3_f32 v83, v83, s21, v82
	v_cvt_pk_fp8_f32 v85, v86, v83 op_sel:[0,0,1]
	v_mul_f32_e32 v83, 0x42800000, v54
	v_mul_f32_e32 v86, 0x42800000, v58
	v_med3_f32 v83, v83, s21, v82
	v_med3_f32 v88, v86, s21, v82

; #define LAS __attribute__((address_space(3)))
; __device__ __forceinline__ float clamp448(float x) { return fminf(fmaxf(x, -448.f), 448.f); }
; __device__ __forceinline__ unsigned pk_fp8x4(float a, float b, float c, float d) {
;     int p = 0; p = __builtin_amdgcn_cvt_pk_fp8_f32(clamp448(a), clamp448(b), p, false); p = __builtin_amdgcn_cvt_pk_fp8_f32(clamp448(c), clamp448(d), p, true); return (unsigned)p; }
; __device__ __forceinline__ void conv8b_run(const Ctx& X, int first, int step, int count) {
;     ...
;         for (int q = 0; q < 4; ++q) { u32x4 o;
;             o.x = pk_fp8x4(v[0][q] * W8_SCALE, v[1][q] * W8_SCALE, v[2][q] * W8_SCALE, v[3][q] * W8_SCALE); o.y = pk_fp8x4(v[4][q] * W8_SCALE, v[5][q] * W8_SCALE, v[6][q] * W8_SCALE, v[7][q] * W8_SCALE);
;             o.z = pk_fp8x4(v[8][q] * W8_SCALE, v[9][q] * W8_SCALE, v[10][q] * W8_SCALE, v[11][q] * W8_SCALE); o.w = pk_fp8x4(v[12][q] * W8_SCALE, v[13][q] * W8_SCALE, v[14][q] * W8_SCALE, v[15][q] * W8_SCALE);
;             *(LAS u32x4*)(buf + (4 * X.lane + q) * CVT_STRIDE + 16 * X.wave) = o; }
	v_cvt_pk_fp8_f32 v86, v83, v88
	v_mul_f32_e32 v87, 0x42800000, v42
	v_mul_f32_e32 v83, 0x42800000, v62
	v_med3_f32 v87, v87, s21, v82
	v_med3_f32 v83, v83, s21, v82
	v_cvt_pk_fp8_f32 v86, v87, v83 op_sel:[0,0,1]
	v_mul_f32_e32 v83, 0x42800000, v26
	v_mul_f32_e32 v87, 0x42800000, v34
	v_med3_f32 v83, v83, s21, v82
	v_med3_f32 v89, v87, s21, v82

; #define LAS __attribute__((address_space(3)))
; __device__ __forceinline__ float clamp448(float x) { return fminf(fmaxf(x, -448.f), 448.f); }
; __device__ __forceinline__ unsigned pk_fp8x4(float a, float b, float c, float d) {
;     int p = 0; p = __builtin_amdgcn_cvt_pk_fp8_f32(clamp448(a), clamp448(b), p, false); p = __builtin_amdgcn_cvt_pk_fp8_f32(clamp448(c), clamp448(d), p, true); return (unsigned)p; }
; __device__ __forceinline__ void conv8b_run(const Ctx& X, int first, int step, int count) {
;     ...
;         for (int q = 0; q < 4; ++q) { u32x4 o;
;             o.x = pk_fp8x4(v[0][q] * W8_SCALE, v[1][q] * W8_SCALE, v[2][q] * W8_SCALE, v[3][q] * W8_SCALE); o.y = pk_fp8x4(v[4][q] * W8_SCALE, v[5][q] * W8_SCALE, v[6][q] * W8_SCALE, v[7][q] * W8_SCALE);
;             o.z = pk_fp8x4(v[8][q] * W8_SCALE, v[9][q] * W8_SCALE, v[10][q] * W8_SCALE, v[11][q] * W8_SCALE); o.w = pk_fp8x4(v[12][q] * W8_SCALE, v[13][q] * W8_SCALE, v[14][q] * W8_SCALE, v[15][q] * W8_SCALE);
;             *(LAS u32x4*)(buf + (4 * X.lane + q) * CVT_STRIDE + 16 * X.wave) = o; }
	v_cvt_pk_fp8_f32 v87, v83, v89
	v_mul_f32_e32 v88, 0x42800000, v10
	v_mul_f32_e32 v83, 0x42800000, v18
	v_med3_f32 v88, v88, s21, v82
	v_med3_f32 v83, v83, s21, v82
	v_cvt_pk_fp8_f32 v87, v88, v83 op_sel:[0,0,1]
	v_mul_f32_e32 v83, 0x42800000, v3
	v_mul_f32_e32 v88, 0x42800000, v15
	v_med3_f32 v83, v83, s21, v82
	v_med3_f32 v90, v88, s21, v82

; #define LAS __attribute__((address_space(3)))
; __device__ __forceinline__ float clamp448(float x) { return fminf(fmaxf(x, -448.f), 448.f); }
; __device__ __forceinline__ unsigned pk_fp8x4(float a, float b, float c, float d) {
;     int p = 0; p = __builtin_amdgcn_cvt_pk_fp8_f32(clamp448(a), clamp448(b), p, false); p = __builtin_amdgcn_cvt_pk_fp8_f32(clamp448(c), clamp448(d), p, true); return (unsigned)p; }
; __device__ __forceinline__ void conv8b_run(const Ctx& X, int first, int step, int count) {
;     ...
;         for (int q = 0; q < 4; ++q) { u32x4 o;
;             o.x = pk_fp8x4(v[0][q] * W8_SCALE, v[1][q] * W8_SCALE, v[2][q] * W8_SCALE, v[3][q] * W8_SCALE); o.y = pk_fp8x4(v[4][q] * W8_SCALE, v[5][q] * W8_SCALE, v[6][q] * W8_SCALE, v[7][q] * W8_SCALE);
;             o.z = pk_fp8x4(v[8][q] * W8_SCALE, v[9][q] * W8_SCALE, v[10][q] * W8_SCALE, v[11][q] * W8_SCALE); o.w = pk_fp8x4(v[12][q] * W8_SCALE, v[13][q] * W8_SCALE, v[14][q] * W8_SCALE, v[15][q] * W8_SCALE);
;             *(LAS u32x4*)(buf + (4 * X.lane + q) * CVT_STRIDE + 16 * X.wave) = o; }
	v_cvt_pk_fp8_f32 v88, v83, v90
	v_mul_f32_e32 v89, 0x42800000, v7
	v_mul_f32_e32 v83, 0x42800000, v31
	v_med3_f32 v89, v89, s21, v82
	v_med3_f32 v83, v83, s21, v82
	v_cvt_pk_fp8_f32 v88, v89, v83 op_sel:[0,0,1]
	v_mul_f32_e32 v83, 0x42800000, v23
	v_mul_f32_e32 v89, 0x42800000, v47
	v_med3_f32 v83, v83, s21, v82
	v_med3_f32 v91, v89, s21, v82

; #define LAS __attribute__((address_space(3)))
; __device__ __forceinline__ float clamp448(float x) { return fminf(fmaxf(x, -448.f), 448.f); }
; __device__ __forceinline__ unsigned pk_fp8x4(float a, float b, float c, float d) {
;     int p = 0; p = __builtin_amdgcn_cvt_pk_fp8_f32(clamp448(a), clamp448(b), p, false); p = __builtin_amdgcn_cvt_pk_fp8_f32(clamp448(c), clamp448(d), p, true); return (unsigned)p; }
; __device__ __forceinline__ void conv8b_run(const Ctx& X, int first, int step, int count) {
;     ...
;         for (int q = 0; q < 4; ++q) { u32x4 o;
;             o.x = pk_fp8x4(v[0][q] * W8_SCALE, v[1][q] * W8_SCALE, v[2][q] * W8_SCALE, v[3][q] * W8_SCALE); o.y = pk_fp8x4(v[4][q] * W8_SCALE, v[5][q] * W8_SCALE, v[6][q] * W8_SCALE, v[7][q] * W8_SCALE);
;             o.z = pk_fp8x4(v[8][q] * W8_SCALE, v[9][q] * W8_SCALE, v[10][q] * W8_SCALE, v[11][q] * W8_SCALE); o.w = pk_fp8x4(v[12][q] * W8_SCALE, v[13][q] * W8_SCALE, v[14][q] * W8_SCALE, v[15][q] * W8_SCALE);
;             *(LAS u32x4*)(buf + (4 * X.lane + q) * CVT_STRIDE + 16 * X.wave) = o; }
	v_cvt_pk_fp8_f32 v89, v83, v91
	v_mul_f32_e32 v90, 0x42800000, v39
	v_mul_f32_e32 v83, 0x42800000, v51
	v_med3_f32 v90, v90, s21, v82
	v_med3_f32 v83, v83, s21, v82
	v_cvt_pk_fp8_f32 v89, v90, v83 op_sel:[0,0,1]
	v_mul_f32_e32 v83, 0x42800000, v55
	v_mul_f32_e32 v90, 0x42800000, v59
	v_med3_f32 v83, v83, s21, v82
	v_med3_f32 v92, v90, s21, v82

; #define LAS __attribute__((address_space(3)))
; __device__ __forceinline__ float clamp448(float x) { return fminf(fmaxf(x, -448.f), 448.f); }
; __device__ __forceinline__ unsigned pk_fp8x4(float a, float b, float c, float d) {
;     int p = 0; p = __builtin_amdgcn_cvt_pk_fp8_f32(clamp448(a), clamp448(b), p, false); p = __builtin_amdgcn_cvt_pk_fp8_f32(clamp448(c), clamp448(d), p, true); return (unsigned)p; }
; __device__ __forceinline__ void conv8b_run(const Ctx& X, int first, int step, int count) {
;     ...
;         for (int q = 0; q < 4; ++q) { u32x4 o;
;             o.x = pk_fp8x4(v[0][q] * W8_SCALE, v[1][q] * W8_SCALE, v[2][q] * W8_SCALE, v[3][q] * W8_SCALE); o.y = pk_fp8x4(v[4][q] * W8_SCALE, v[5][q] * W8_SCALE, v[6][q] * W8_SCALE, v[7][q] * W8_SCALE);
;             o.z = pk_fp8x4(v[8][q] * W8_SCALE, v[9][q] * W8_SCALE, v[10][q] * W8_SCALE, v[11][q] * W8_SCALE); o.w = pk_fp8x4(v[12][q] * W8_SCALE, v[13][q] * W8_SCALE, v[14][q] * W8_SCALE, v[15][q] * W8_SCALE);
;             *(LAS u32x4*)(buf + (4 * X.lane + q) * CVT_STRIDE + 16 * X.wave) = o; }
	v_cvt_pk_fp8_f32 v90, v83, v92
	v_mul_f32_e32 v91, 0x42800000, v43
	v_mul_f32_e32 v83, 0x42800000, v63
	v_med3_f32 v91, v91, s21, v82
	v_med3_f32 v83, v83, s21, v82
	v_cvt_pk_fp8_f32 v90, v91, v83 op_sel:[0,0,1]
	v_mul_f32_e32 v83, 0x42800000, v27
	v_mul_f32_e32 v91, 0x42800000, v35
	v_med3_f32 v83, v83, s21, v82
	v_med3_f32 v93, v91, s21, v82

; #define LAS __attribute__((address_space(3)))
; __device__ __forceinline__ float clamp448(float x) { return fminf(fmaxf(x, -448.f), 448.f); }
; __device__ __forceinline__ unsigned pk_fp8x4(float a, float b, float c, float d) {
;     int p = 0; p = __builtin_amdgcn_cvt_pk_fp8_f32(clamp448(a), clamp448(b), p, false); p = __builtin_amdgcn_cvt_pk_fp8_f32(clamp448(c), clamp448(d), p, true); return (unsigned)p; }
; __device__ __forceinline__ void conv8b_run(const Ctx& X, int first, int step, int count) {
;     ...
;         for (int q = 0; q < 4; ++q) { u32x4 o;
;             o.x = pk_fp8x4(v[0][q] * W8_SCALE, v[1][q] * W8_SCALE, v[2][q] * W8_SCALE, v[3][q] * W8_SCALE); o.y = pk_fp8x4(v[4][q] * W8_SCALE, v[5][q] * W8_SCALE, v[6][q] * W8_SCALE, v[7][q] * W8_SCALE);
;             o.z = pk_fp8x4(v[8][q] * W8_SCALE, v[9][q] * W8_SCALE, v[10][q] * W8_SCALE, v[11][q] * W8_SCALE); o.w = pk_fp8x4(v[12][q] * W8_SCALE, v[13][q] * W8_SCALE, v[14][q] * W8_SCALE, v[15][q] * W8_SCALE);
;             *(LAS u32x4*)(buf + (4 * X.lane + q) * CVT_STRIDE + 16 * X.wave) = o; }
	v_cvt_pk_fp8_f32 v91, v83, v93
	s_bitcmp1_b32 s6, 0
	v_mul_f32_e32 v92, 0x42800000, v11
	v_mul_f32_e32 v83, 0x42800000, v19
	s_cselect_b32 s8, 0x9000, 0
	v_med3_f32 v92, v92, s21, v82
	v_med3_f32 v83, v83, s21, v82
	s_add_i32 s24, s8, 0
	v_cvt_pk_fp8_f32 v91, v92, v83 op_sel:[0,0,1]
	s_add_i32 s8, s19, s24
	v_add_u32_e32 v83, s8, v78
	ds_write_b128 v83, v[84:87]
	ds_write_b128 v83, v[88:91] offset:144
	v_mul_f32_e32 v84, 0x42800000, v4
	v_mul_f32_e32 v85, 0x42800000, v16
	v_med3_f32 v87, v84, s21, v82
	v_med3_f32 v85, v85, s21, v82

; #define LAS __attribute__((address_space(3)))
; __device__ __forceinline__ float clamp448(float x) { return fminf(fmaxf(x, -448.f), 448.f); }
; __device__ __forceinline__ unsigned pk_fp8x4(float a, float b, float c, float d) {
;     int p = 0; p = __builtin_amdgcn_cvt_pk_fp8_f32(clamp448(a), clamp448(b), p, false); p = __builtin_amdgcn_cvt_pk_fp8_f32(clamp448(c), clamp448(d), p, true); return (unsigned)p; }
; __device__ __forceinline__ void conv8b_run(const Ctx& X, int first, int step, int count) {
;     ...
;         for (int q = 0; q < 4; ++q) { u32x4 o;
;             o.x = pk_fp8x4(v[0][q] * W8_SCALE, v[1][q] * W8_SCALE, v[2][q] * W8_SCALE, v[3][q] * W8_SCALE); o.y = pk_fp8x4(v[4][q] * W8_SCALE, v[5][q] * W8_SCALE, v[6][q] * W8_SCALE, v[7][q] * W8_SCALE);
;             o.z = pk_fp8x4(v[8][q] * W8_SCALE, v[9][q] * W8_SCALE, v[10][q] * W8_SCALE, v[11][q] * W8_SCALE); o.w = pk_fp8x4(v[12][q] * W8_SCALE, v[13][q] * W8_SCALE, v[14][q] * W8_SCALE, v[15][q] * W8_SCALE);
;             *(LAS u32x4*)(buf + (4 * X.lane + q) * CVT_STRIDE + 16 * X.wave) = o; }
	v_cvt_pk_fp8_f32 v84, v87, v85
	v_mul_f32_e32 v86, 0x42800000, v8
	v_mul_f32_e32 v85, 0x42800000, v32
	v_med3_f32 v86, v86, s21, v82
	v_med3_f32 v85, v85, s21, v82
	v_cvt_pk_fp8_f32 v84, v86, v85 op_sel:[0,0,1]
	v_mul_f32_e32 v85, 0x42800000, v24
	v_mul_f32_e32 v86, 0x42800000, v48
	v_med3_f32 v88, v85, s21, v82
	v_med3_f32 v86, v86, s21, v82

; #define LAS __attribute__((address_space(3)))
; __device__ __forceinline__ float clamp448(float x) { return fminf(fmaxf(x, -448.f), 448.f); }
; __device__ __forceinline__ unsigned pk_fp8x4(float a, float b, float c, float d) {
;     int p = 0; p = __builtin_amdgcn_cvt_pk_fp8_f32(clamp448(a), clamp448(b), p, false); p = __builtin_amdgcn_cvt_pk_fp8_f32(clamp448(c), clamp448(d), p, true); return (unsigned)p; }
; __device__ __forceinline__ void conv8b_run(const Ctx& X, int first, int step, int count) {
;     ...
;         for (int q = 0; q < 4; ++q) { u32x4 o;
;             o.x = pk_fp8x4(v[0][q] * W8_SCALE, v[1][q] * W8_SCALE, v[2][q] * W8_SCALE, v[3][q] * W8_SCALE); o.y = pk_fp8x4(v[4][q] * W8_SCALE, v[5][q] * W8_SCALE, v[6][q] * W8_SCALE, v[7][q] * W8_SCALE);
;             o.z = pk_fp8x4(v[8][q] * W8_SCALE, v[9][q] * W8_SCALE, v[10][q] * W8_SCALE, v[11][q] * W8_SCALE); o.w = pk_fp8x4(v[12][q] * W8_SCALE, v[13][q] * W8_SCALE, v[14][q] * W8_SCALE, v[15][q] * W8_SCALE);
;             *(LAS u32x4*)(buf + (4 * X.lane + q) * CVT_STRIDE + 16 * X.wave) = o; }
	v_cvt_pk_fp8_f32 v85, v88, v86
	v_mul_f32_e32 v87, 0x42800000, v40
	v_mul_f32_e32 v86, 0x42800000, v52
	v_med3_f32 v87, v87, s21, v82
	v_med3_f32 v86, v86, s21, v82
	v_cvt_pk_fp8_f32 v85, v87, v86 op_sel:[0,0,1]
	v_mul_f32_e32 v86, 0x42800000, v56
	v_mul_f32_e32 v87, 0x42800000, v60
	v_med3_f32 v89, v86, s21, v82
	v_med3_f32 v87, v87, s21, v82

; #define LAS __attribute__((address_space(3)))
; __device__ __forceinline__ float clamp448(float x) { return fminf(fmaxf(x, -448.f), 448.f); }
; __device__ __forceinline__ unsigned pk_fp8x4(float a, float b, float c, float d) {
;     int p = 0; p = __builtin_amdgcn_cvt_pk_fp8_f32(clamp448(a), clamp448(b), p, false); p = __builtin_amdgcn_cvt_pk_fp8_f32(clamp448(c), clamp448(d), p, true); return (unsigned)p; }
; __device__ __forceinline__ void conv8b_run(const Ctx& X, int first, int step, int count) {
;     ...
;         for (int q = 0; q < 4; ++q) { u32x4 o;
;             o.x = pk_fp8x4(v[0][q] * W8_SCALE, v[1][q] * W8_SCALE, v[2][q] * W8_SCALE, v[3][q] * W8_SCALE); o.y = pk_fp8x4(v[4][q] * W8_SCALE, v[5][q] * W8_SCALE, v[6][q] * W8_SCALE, v[7][q] * W8_SCALE);
;             o.z = pk_fp8x4(v[8][q] * W8_SCALE, v[9][q] * W8_SCALE, v[10][q] * W8_SCALE, v[11][q] * W8_SCALE); o.w = pk_fp8x4(v[12][q] * W8_SCALE, v[13][q] * W8_SCALE, v[14][q] * W8_SCALE, v[15][q] * W8_SCALE);
;             *(LAS u32x4*)(buf + (4 * X.lane + q) * CVT_STRIDE + 16 * X.wave) = o; }
	v_cvt_pk_fp8_f32 v86, v89, v87
	v_mul_f32_e32 v88, 0x42800000, v44
	v_mul_f32_e32 v87, 0x42800000, v64
	v_med3_f32 v88, v88, s21, v82
	v_med3_f32 v87, v87, s21, v82
	v_cvt_pk_fp8_f32 v86, v88, v87 op_sel:[0,0,1]
	v_mul_f32_e32 v87, 0x42800000, v28
	v_mul_f32_e32 v88, 0x42800000, v36
	v_med3_f32 v90, v87, s21, v82
	v_med3_f32 v88, v88, s21, v82

; #define LAS __attribute__((address_space(3)))
; __device__ __forceinline__ float clamp448(float x) { return fminf(fmaxf(x, -448.f), 448.f); }
; __device__ __forceinline__ unsigned pk_fp8x4(float a, float b, float c, float d) {
;     int p = 0; p = __builtin_amdgcn_cvt_pk_fp8_f32(clamp448(a), clamp448(b), p, false); p = __builtin_amdgcn_cvt_pk_fp8_f32(clamp448(c), clamp448(d), p, true); return (unsigned)p; }
; __device__ __forceinline__ void conv8b_run(const Ctx& X, int first, int step, int count) {
;     ...
;         for (int q = 0; q < 4; ++q) { u32x4 o;
;             o.x = pk_fp8x4(v[0][q] * W8_SCALE, v[1][q] * W8_SCALE, v[2][q] * W8_SCALE, v[3][q] * W8_SCALE); o.y = pk_fp8x4(v[4][q] * W8_SCALE, v[5][q] * W8_SCALE, v[6][q] * W8_SCALE, v[7][q] * W8_SCALE);
;             o.z = pk_fp8x4(v[8][q] * W8_SCALE, v[9][q] * W8_SCALE, v[10][q] * W8_SCALE, v[11][q] * W8_SCALE); o.w = pk_fp8x4(v[12][q] * W8_SCALE, v[13][q] * W8_SCALE, v[14][q] * W8_SCALE, v[15][q] * W8_SCALE);
;             *(LAS u32x4*)(buf + (4 * X.lane + q) * CVT_STRIDE + 16 * X.wave) = o; }
	v_cvt_pk_fp8_f32 v87, v90, v88
	v_mul_f32_e32 v89, 0x42800000, v12
	v_mul_f32_e32 v88, 0x42800000, v20
	v_med3_f32 v89, v89, s21, v82
	v_med3_f32 v88, v88, s21, v82
	v_cvt_pk_fp8_f32 v87, v89, v88 op_sel:[0,0,1]
	v_mul_f32_e32 v88, 0x42800000, v5
	v_mul_f32_e32 v89, 0x42800000, v17
	v_med3_f32 v91, v88, s21, v82
	v_med3_f32 v89, v89, s21, v82

; #define LAS __attribute__((address_space(3)))
; __device__ __forceinline__ float clamp448(float x) { return fminf(fmaxf(x, -448.f), 448.f); }
; __device__ __forceinline__ unsigned pk_fp8x4(float a, float b, float c, float d) {
;     int p = 0; p = __builtin_amdgcn_cvt_pk_fp8_f32(clamp448(a), clamp448(b), p, false); p = __builtin_amdgcn_cvt_pk_fp8_f32(clamp448(c), clamp448(d), p, true); return (unsigned)p; }
; __device__ __forceinline__ void conv8b_run(const Ctx& X, int first, int step, int count) {
;     ...
;         for (int q = 0; q < 4; ++q) { u32x4 o;
;             o.x = pk_fp8x4(v[0][q] * W8_SCALE, v[1][q] * W8_SCALE, v[2][q] * W8_SCALE, v[3][q] * W8_SCALE); o.y = pk_fp8x4(v[4][q] * W8_SCALE, v[5][q] * W8_SCALE, v[6][q] * W8_SCALE, v[7][q] * W8_SCALE);
;             o.z = pk_fp8x4(v[8][q] * W8_SCALE, v[9][q] * W8_SCALE, v[10][q] * W8_SCALE, v[11][q] * W8_SCALE); o.w = pk_fp8x4(v[12][q] * W8_SCALE, v[13][q] * W8_SCALE, v[14][q] * W8_SCALE, v[15][q] * W8_SCALE);
;             *(LAS u32x4*)(buf + (4 * X.lane + q) * CVT_STRIDE + 16 * X.wave) = o; }
	v_cvt_pk_fp8_f32 v88, v91, v89
	v_mul_f32_e32 v90, 0x42800000, v9
	v_mul_f32_e32 v89, 0x42800000, v33
	v_med3_f32 v90, v90, s21, v82
	v_med3_f32 v89, v89, s21, v82
	v_cvt_pk_fp8_f32 v88, v90, v89 op_sel:[0,0,1]
	v_mul_f32_e32 v89, 0x42800000, v25
	v_mul_f32_e32 v90, 0x42800000, v49
	v_med3_f32 v92, v89, s21, v82
	v_med3_f32 v90, v90, s21, v82

; #define LAS __attribute__((address_space(3)))
; __device__ __forceinline__ float clamp448(float x) { return fminf(fmaxf(x, -448.f), 448.f); }
; __device__ __forceinline__ unsigned pk_fp8x4(float a, float b, float c, float d) {
;     int p = 0; p = __builtin_amdgcn_cvt_pk_fp8_f32(clamp448(a), clamp448(b), p, false); p = __builtin_amdgcn_cvt_pk_fp8_f32(clamp448(c), clamp448(d), p, true); return (unsigned)p; }
; __device__ __forceinline__ void conv8b_run(const Ctx& X, int first, int step, int count) {
;     ...
;         for (int q = 0; q < 4; ++q) { u32x4 o;
;             o.x = pk_fp8x4(v[0][q] * W8_SCALE, v[1][q] * W8_SCALE, v[2][q] * W8_SCALE, v[3][q] * W8_SCALE); o.y = pk_fp8x4(v[4][q] * W8_SCALE, v[5][q] * W8_SCALE, v[6][q] * W8_SCALE, v[7][q] * W8_SCALE);
;             o.z = pk_fp8x4(v[8][q] * W8_SCALE, v[9][q] * W8_SCALE, v[10][q] * W8_SCALE, v[11][q] * W8_SCALE); o.w = pk_fp8x4(v[12][q] * W8_SCALE, v[13][q] * W8_SCALE, v[14][q] * W8_SCALE, v[15][q] * W8_SCALE);
;             *(LAS u32x4*)(buf + (4 * X.lane + q) * CVT_STRIDE + 16 * X.wave) = o; }
	v_cvt_pk_fp8_f32 v89, v92, v90
	v_mul_f32_e32 v91, 0x42800000, v41
	v_mul_f32_e32 v90, 0x42800000, v53
	v_med3_f32 v91, v91, s21, v82
	v_med3_f32 v90, v90, s21, v82
	v_cvt_pk_fp8_f32 v89, v91, v90 op_sel:[0,0,1]
	v_mul_f32_e32 v90, 0x42800000, v57
	v_mul_f32_e32 v91, 0x42800000, v61
	v_med3_f32 v93, v90, s21, v82
	v_med3_f32 v91, v91, s21, v82

; #define LAS __attribute__((address_space(3)))
; __device__ __forceinline__ float clamp448(float x) { return fminf(fmaxf(x, -448.f), 448.f); }
; __device__ __forceinline__ unsigned pk_fp8x4(float a, float b, float c, float d) {
;     int p = 0; p = __builtin_amdgcn_cvt_pk_fp8_f32(clamp448(a), clamp448(b), p, false); p = __builtin_amdgcn_cvt_pk_fp8_f32(clamp448(c), clamp448(d), p, true); return (unsigned)p; }
; __device__ __forceinline__ void conv8b_run(const Ctx& X, int first, int step, int count) {
;     ...
;         for (int q = 0; q < 4; ++q) { u32x4 o;
;             o.x = pk_fp8x4(v[0][q] * W8_SCALE, v[1][q] * W8_SCALE, v[2][q] * W8_SCALE, v[3][q] * W8_SCALE); o.y = pk_fp8x4(v[4][q] * W8_SCALE, v[5][q] * W8_SCALE, v[6][q] * W8_SCALE, v[7][q] * W8_SCALE);
;             o.z = pk_fp8x4(v[8][q] * W8_SCALE, v[9][q] * W8_SCALE, v[10][q] * W8_SCALE, v[11][q] * W8_SCALE); o.w = pk_fp8x4(v[12][q] * W8_SCALE, v[13][q] * W8_SCALE, v[14][q] * W8_SCALE, v[15][q] * W8_SCALE);
;             *(LAS u32x4*)(buf + (4 * X.lane + q) * CVT_STRIDE + 16 * X.wave) = o; }
	v_cvt_pk_fp8_f32 v90, v93, v91
	v_mul_f32_e32 v92, 0x42800000, v45
	v_mul_f32_e32 v91, 0x42800000, v65
	v_med3_f32 v92, v92, s21, v82
	v_med3_f32 v91, v91, s21, v82
	v_cvt_pk_fp8_f32 v90, v92, v91 op_sel:[0,0,1]
	v_mul_f32_e32 v91, 0x42800000, v29
	v_mul_f32_e32 v92, 0x42800000, v37
	v_med3_f32 v94, v91, s21, v82
	v_med3_f32 v92, v92, s21, v82

; #define LAS __attribute__((address_space(3)))
; __device__ __forceinline__ Cvb conv8b_dec(const Ctx& X, int bit) { Cvb c; int kb, nb;
;     if (bit < I_GU8 / 8) { const int e = bit >> 8, r = bit & 255; kb = r >> 4; nb = r & 15; c.N = 2 * DFF; c.W = XP_w_gu(X) + (size_t)e * D * (2 * DFF); c.WT = XP_WguT(X) + (size_t)e * 16 * PAN_GU + (size_t)kb * PAN_GU; }
;     else { const int b2 = bit - I_GU8 / 8, e = b2 >> 7, r = b2 & 127; kb = r >> 3; nb = r & 7; c.N = D; c.W = XP_w_d(X) + (size_t)e * DFF * D; c.WT = XP_WdT(X) + (size_t)e * 16 * PAN_D + (size_t)kb * PAN_D; }
;     c.W += (size_t)(kb * 128 + 16 * X.wave) * c.N + nb * 256 + 4 * X.lane;
;     c.WT += (size_t)(nb * 256 + 32 * X.wave + (X.lane >> 3)) * 128 + 16 * (X.lane & 7);
; __device__ __forceinline__ void conv8b_run(const Ctx& X, int first, int step, int count) {
;     ...
;         for (int q = 0; q < 4; ++q) { u32x4 o;
;             o.x = pk_fp8x4(v[0][q] * W8_SCALE, v[1][q] * W8_SCALE, v[2][q] * W8_SCALE, v[3][q] * W8_SCALE); o.y = pk_fp8x4(v[4][q] * W8_SCALE, v[5][q] * W8_SCALE, v[6][q] * W8_SCALE, v[7][q] * W8_SCALE);
;             o.z = pk_fp8x4(v[8][q] * W8_SCALE, v[9][q] * W8_SCALE, v[10][q] * W8_SCALE, v[11][q] * W8_SCALE); o.w = pk_fp8x4(v[12][q] * W8_SCALE, v[13][q] * W8_SCALE, v[14][q] * W8_SCALE, v[15][q] * W8_SCALE);
;             *(LAS u32x4*)(buf + (4 * X.lane + q) * CVT_STRIDE + 16 * X.wave) = o; }
;         if (j + 1 < count) { cn = conv8b_dec(X, first + (j + 1) * step);
; #pragma unroll
;             for (int i = 0; i < 16; ++i) v[i] = __builtin_nontemporal_load((const f32x4*)(cn.W + (size_t)i * cn.N)); }
	v_cvt_pk_fp8_f32 v91, v94, v92
	v_mul_f32_e32 v93, 0x42800000, v13
	v_mul_f32_e32 v92, 0x42800000, v21
	v_med3_f32 v93, v93, s21, v82
	v_med3_f32 v92, v92, s21, v82
	v_cvt_pk_fp8_f32 v91, v93, v92 op_sel:[0,0,1]
	s_add_i32 s25, s6, 1
	s_cmp_ge_i32 s25, s23
	ds_write_b128 v83, v[84:87] offset:288
	ds_write_b128 v83, v[88:91] offset:432
	s_cbranch_scc1 .LBB0_140
	s_add_i32 s29, s22, s6
	s_add_i32 s28, s29, 1
	s_cmpk_gt_i32 s28, 0x1fff
	s_mov_b64 s[12:13], -1
	s_cbranch_scc0 .LBB0_144
	s_mov_b64 s[8:9], s[100:101]
	s_addk_i32 s29, 0xe001
	s_lshr_b32 s6, s29, 7
	s_bfe_u32 s27, s28, 0x40003
	s_and_b32 s26, s28, 7
	s_lshl_b64 s[10:11], s[6:7], 24
	s_waitcnt lgkmcnt(0)
	s_add_u32 s8, s8, s10
	s_addc_u32 s9, s9, s11
	s_lshl_b64 s[10:11], s[6:7], 22
	s_add_u32 s10, s15, s10
	s_addc_u32 s11, s16, s11
	s_lshl_b32 s6, s27, 18
	s_mov_b64 s[12:13], 0

; #define LAS __attribute__((address_space(3)))
; __device__ __forceinline__ float clamp448(float x) { return fminf(fmaxf(x, -448.f), 448.f); }
; __device__ __forceinline__ unsigned pk_fp8x4(float a, float b, float c, float d) {
;     int p = 0; p = __builtin_amdgcn_cvt_pk_fp8_f32(clamp448(a), clamp448(b), p, false); p = __builtin_amdgcn_cvt_pk_fp8_f32(clamp448(c), clamp448(d), p, true); return (unsigned)p; }
; __device__ __forceinline__ void conv8b_run(const Ctx& X, int first, int step, int count) {
;     ...
;         for (int q = 0; q < 4; ++q) { u32x4 o;
;             o.x = pk_fp8x4(v[0][q] * W8_SCALE, v[1][q] * W8_SCALE, v[2][q] * W8_SCALE, v[3][q] * W8_SCALE); o.y = pk_fp8x4(v[4][q] * W8_SCALE, v[5][q] * W8_SCALE, v[6][q] * W8_SCALE, v[7][q] * W8_SCALE);
;             o.z = pk_fp8x4(v[8][q] * W8_SCALE, v[9][q] * W8_SCALE, v[10][q] * W8_SCALE, v[11][q] * W8_SCALE); o.w = pk_fp8x4(v[12][q] * W8_SCALE, v[13][q] * W8_SCALE, v[14][q] * W8_SCALE, v[15][q] * W8_SCALE);
;             *(LAS u32x4*)(buf + (4 * X.lane + q) * CVT_STRIDE + 16 * X.wave) = o; }
.LBB0_477:
	s_waitcnt vmcnt(4)
	v_mul_f32_e32 v79, 0x42800000, v62
	v_mul_f32_e32 v80, 0x42800000, v30
	v_med3_f32 v79, v79, s14, v78
	v_med3_f32 v82, v80, s14, v78

; #define LAS __attribute__((address_space(3)))
; __device__ __forceinline__ float clamp448(float x) { return fminf(fmaxf(x, -448.f), 448.f); }
; __device__ __forceinline__ unsigned pk_fp8x4(float a, float b, float c, float d) {
;     int p = 0; p = __builtin_amdgcn_cvt_pk_fp8_f32(clamp448(a), clamp448(b), p, false); p = __builtin_amdgcn_cvt_pk_fp8_f32(clamp448(c), clamp448(d), p, true); return (unsigned)p; }
; __device__ __forceinline__ void conv8b_run(const Ctx& X, int first, int step, int count) {
;     ...
;         for (int q = 0; q < 4; ++q) { u32x4 o;
;             o.x = pk_fp8x4(v[0][q] * W8_SCALE, v[1][q] * W8_SCALE, v[2][q] * W8_SCALE, v[3][q] * W8_SCALE); o.y = pk_fp8x4(v[4][q] * W8_SCALE, v[5][q] * W8_SCALE, v[6][q] * W8_SCALE, v[7][q] * W8_SCALE);
;             o.z = pk_fp8x4(v[8][q] * W8_SCALE, v[9][q] * W8_SCALE, v[10][q] * W8_SCALE, v[11][q] * W8_SCALE); o.w = pk_fp8x4(v[12][q] * W8_SCALE, v[13][q] * W8_SCALE, v[14][q] * W8_SCALE, v[15][q] * W8_SCALE);
;             *(LAS u32x4*)(buf + (4 * X.lane + q) * CVT_STRIDE + 16 * X.wave) = o; }
	v_cvt_pk_fp8_f32 v80, v79, v82
	v_mul_f32_e32 v81, 0x42800000, v26
	v_mul_f32_e32 v79, 0x42800000, v58
	v_med3_f32 v81, v81, s14, v78
	v_med3_f32 v79, v79, s14, v78
	v_cvt_pk_fp8_f32 v80, v81, v79 op_sel:[0,0,1]
	v_mul_f32_e32 v79, 0x42800000, v22
	v_mul_f32_e32 v81, 0x42800000, v54
	v_med3_f32 v79, v79, s14, v78
	v_med3_f32 v83, v81, s14, v78

; #define LAS __attribute__((address_space(3)))
; __device__ __forceinline__ float clamp448(float x) { return fminf(fmaxf(x, -448.f), 448.f); }
; __device__ __forceinline__ unsigned pk_fp8x4(float a, float b, float c, float d) {
;     int p = 0; p = __builtin_amdgcn_cvt_pk_fp8_f32(clamp448(a), clamp448(b), p, false); p = __builtin_amdgcn_cvt_pk_fp8_f32(clamp448(c), clamp448(d), p, true); return (unsigned)p; }
; __device__ __forceinline__ void conv8b_run(const Ctx& X, int first, int step, int count) {
;     ...
;         for (int q = 0; q < 4; ++q) { u32x4 o;
;             o.x = pk_fp8x4(v[0][q] * W8_SCALE, v[1][q] * W8_SCALE, v[2][q] * W8_SCALE, v[3][q] * W8_SCALE); o.y = pk_fp8x4(v[4][q] * W8_SCALE, v[5][q] * W8_SCALE, v[6][q] * W8_SCALE, v[7][q] * W8_SCALE);
;             o.z = pk_fp8x4(v[8][q] * W8_SCALE, v[9][q] * W8_SCALE, v[10][q] * W8_SCALE, v[11][q] * W8_SCALE); o.w = pk_fp8x4(v[12][q] * W8_SCALE, v[13][q] * W8_SCALE, v[14][q] * W8_SCALE, v[15][q] * W8_SCALE);
;             *(LAS u32x4*)(buf + (4 * X.lane + q) * CVT_STRIDE + 16 * X.wave) = o; }
	v_cvt_pk_fp8_f32 v81, v79, v83
	v_mul_f32_e32 v82, 0x42800000, v18
	v_mul_f32_e32 v79, 0x42800000, v50
	v_med3_f32 v82, v82, s14, v78
	v_med3_f32 v79, v79, s14, v78
	v_cvt_pk_fp8_f32 v81, v82, v79 op_sel:[0,0,1]
	v_mul_f32_e32 v79, 0x42800000, v14
	v_mul_f32_e32 v82, 0x42800000, v46
	v_med3_f32 v79, v79, s14, v78
	v_med3_f32 v84, v82, s14, v78

; #define LAS __attribute__((address_space(3)))
; __device__ __forceinline__ float clamp448(float x) { return fminf(fmaxf(x, -448.f), 448.f); }
; __device__ __forceinline__ unsigned pk_fp8x4(float a, float b, float c, float d) {
;     int p = 0; p = __builtin_amdgcn_cvt_pk_fp8_f32(clamp448(a), clamp448(b), p, false); p = __builtin_amdgcn_cvt_pk_fp8_f32(clamp448(c), clamp448(d), p, true); return (unsigned)p; }
; __device__ __forceinline__ void conv8b_run(const Ctx& X, int first, int step, int count) {
;     ...
;         for (int q = 0; q < 4; ++q) { u32x4 o;
;             o.x = pk_fp8x4(v[0][q] * W8_SCALE, v[1][q] * W8_SCALE, v[2][q] * W8_SCALE, v[3][q] * W8_SCALE); o.y = pk_fp8x4(v[4][q] * W8_SCALE, v[5][q] * W8_SCALE, v[6][q] * W8_SCALE, v[7][q] * W8_SCALE);
;             o.z = pk_fp8x4(v[8][q] * W8_SCALE, v[9][q] * W8_SCALE, v[10][q] * W8_SCALE, v[11][q] * W8_SCALE); o.w = pk_fp8x4(v[12][q] * W8_SCALE, v[13][q] * W8_SCALE, v[14][q] * W8_SCALE, v[15][q] * W8_SCALE);
;             *(LAS u32x4*)(buf + (4 * X.lane + q) * CVT_STRIDE + 16 * X.wave) = o; }
	v_cvt_pk_fp8_f32 v82, v79, v84
	v_mul_f32_e32 v83, 0x42800000, v10
	v_mul_f32_e32 v79, 0x42800000, v42
	v_med3_f32 v83, v83, s14, v78
	v_med3_f32 v79, v79, s14, v78
	v_cvt_pk_fp8_f32 v82, v83, v79 op_sel:[0,0,1]
	v_mul_f32_e32 v79, 0x42800000, v6
	v_mul_f32_e32 v83, 0x42800000, v38
	v_med3_f32 v79, v79, s14, v78
	v_med3_f32 v85, v83, s14, v78

; #define LAS __attribute__((address_space(3)))
; __device__ __forceinline__ float clamp448(float x) { return fminf(fmaxf(x, -448.f), 448.f); }
; __device__ __forceinline__ unsigned pk_fp8x4(float a, float b, float c, float d) {
;     int p = 0; p = __builtin_amdgcn_cvt_pk_fp8_f32(clamp448(a), clamp448(b), p, false); p = __builtin_amdgcn_cvt_pk_fp8_f32(clamp448(c), clamp448(d), p, true); return (unsigned)p; }
; __device__ __forceinline__ void conv8b_run(const Ctx& X, int first, int step, int count) {
;     ...
;         for (int q = 0; q < 4; ++q) { u32x4 o;
;             o.x = pk_fp8x4(v[0][q] * W8_SCALE, v[1][q] * W8_SCALE, v[2][q] * W8_SCALE, v[3][q] * W8_SCALE); o.y = pk_fp8x4(v[4][q] * W8_SCALE, v[5][q] * W8_SCALE, v[6][q] * W8_SCALE, v[7][q] * W8_SCALE);
;             o.z = pk_fp8x4(v[8][q] * W8_SCALE, v[9][q] * W8_SCALE, v[10][q] * W8_SCALE, v[11][q] * W8_SCALE); o.w = pk_fp8x4(v[12][q] * W8_SCALE, v[13][q] * W8_SCALE, v[14][q] * W8_SCALE, v[15][q] * W8_SCALE);
;             *(LAS u32x4*)(buf + (4 * X.lane + q) * CVT_STRIDE + 16 * X.wave) = o; }
	v_cvt_pk_fp8_f32 v83, v79, v85
	v_mul_f32_e32 v84, 0x42800000, v2
	v_mul_f32_e32 v79, 0x42800000, v34
	s_bitcmp1_b32 s16, 0
	v_med3_f32 v84, v84, s14, v78
	v_med3_f32 v79, v79, s14, v78
	s_cselect_b32 s2, 0x9000, 0
	v_cvt_pk_fp8_f32 v83, v84, v79 op_sel:[0,0,1]
	s_add_i32 s17, s2, 0
	s_add_i32 s2, s12, s17
	v_add_u32_e32 v79, s2, v76
	ds_write_b128 v79, v[80:83]
	v_mul_f32_e32 v80, 0x42800000, v63
	v_mul_f32_e32 v81, 0x42800000, v31
	v_med3_f32 v83, v80, s14, v78
	v_med3_f32 v81, v81, s14, v78

; #define LAS __attribute__((address_space(3)))
; __device__ __forceinline__ float clamp448(float x) { return fminf(fmaxf(x, -448.f), 448.f); }
; __device__ __forceinline__ unsigned pk_fp8x4(float a, float b, float c, float d) {
;     int p = 0; p = __builtin_amdgcn_cvt_pk_fp8_f32(clamp448(a), clamp448(b), p, false); p = __builtin_amdgcn_cvt_pk_fp8_f32(clamp448(c), clamp448(d), p, true); return (unsigned)p; }
; __device__ __forceinline__ void conv8b_run(const Ctx& X, int first, int step, int count) {
;     ...
;         for (int q = 0; q < 4; ++q) { u32x4 o;
;             o.x = pk_fp8x4(v[0][q] * W8_SCALE, v[1][q] * W8_SCALE, v[2][q] * W8_SCALE, v[3][q] * W8_SCALE); o.y = pk_fp8x4(v[4][q] * W8_SCALE, v[5][q] * W8_SCALE, v[6][q] * W8_SCALE, v[7][q] * W8_SCALE);
;             o.z = pk_fp8x4(v[8][q] * W8_SCALE, v[9][q] * W8_SCALE, v[10][q] * W8_SCALE, v[11][q] * W8_SCALE); o.w = pk_fp8x4(v[12][q] * W8_SCALE, v[13][q] * W8_SCALE, v[14][q] * W8_SCALE, v[15][q] * W8_SCALE);
;             *(LAS u32x4*)(buf + (4 * X.lane + q) * CVT_STRIDE + 16 * X.wave) = o; }
	v_cvt_pk_fp8_f32 v80, v83, v81
	v_mul_f32_e32 v82, 0x42800000, v27
	v_mul_f32_e32 v81, 0x42800000, v59
	v_med3_f32 v82, v82, s14, v78
	v_med3_f32 v81, v81, s14, v78
	v_cvt_pk_fp8_f32 v80, v82, v81 op_sel:[0,0,1]
	v_mul_f32_e32 v81, 0x42800000, v23
	v_mul_f32_e32 v82, 0x42800000, v55
	v_med3_f32 v84, v81, s14, v78
	v_med3_f32 v82, v82, s14, v78

; #define LAS __attribute__((address_space(3)))
; __device__ __forceinline__ float clamp448(float x) { return fminf(fmaxf(x, -448.f), 448.f); }
; __device__ __forceinline__ unsigned pk_fp8x4(float a, float b, float c, float d) {
;     int p = 0; p = __builtin_amdgcn_cvt_pk_fp8_f32(clamp448(a), clamp448(b), p, false); p = __builtin_amdgcn_cvt_pk_fp8_f32(clamp448(c), clamp448(d), p, true); return (unsigned)p; }
; __device__ __forceinline__ void conv8b_run(const Ctx& X, int first, int step, int count) {
;     ...
;         for (int q = 0; q < 4; ++q) { u32x4 o;
;             o.x = pk_fp8x4(v[0][q] * W8_SCALE, v[1][q] * W8_SCALE, v[2][q] * W8_SCALE, v[3][q] * W8_SCALE); o.y = pk_fp8x4(v[4][q] * W8_SCALE, v[5][q] * W8_SCALE, v[6][q] * W8_SCALE, v[7][q] * W8_SCALE);
;             o.z = pk_fp8x4(v[8][q] * W8_SCALE, v[9][q] * W8_SCALE, v[10][q] * W8_SCALE, v[11][q] * W8_SCALE); o.w = pk_fp8x4(v[12][q] * W8_SCALE, v[13][q] * W8_SCALE, v[14][q] * W8_SCALE, v[15][q] * W8_SCALE);
;             *(LAS u32x4*)(buf + (4 * X.lane + q) * CVT_STRIDE + 16 * X.wave) = o; }
	v_cvt_pk_fp8_f32 v81, v84, v82
	v_mul_f32_e32 v83, 0x42800000, v19
	v_mul_f32_e32 v82, 0x42800000, v51
	v_med3_f32 v83, v83, s14, v78
	v_med3_f32 v82, v82, s14, v78
	v_cvt_pk_fp8_f32 v81, v83, v82 op_sel:[0,0,1]
	v_mul_f32_e32 v82, 0x42800000, v15
	v_mul_f32_e32 v83, 0x42800000, v47
	v_med3_f32 v85, v82, s14, v78
	v_med3_f32 v83, v83, s14, v78

; #define LAS __attribute__((address_space(3)))
; __device__ __forceinline__ float clamp448(float x) { return fminf(fmaxf(x, -448.f), 448.f); }
; __device__ __forceinline__ unsigned pk_fp8x4(float a, float b, float c, float d) {
;     int p = 0; p = __builtin_amdgcn_cvt_pk_fp8_f32(clamp448(a), clamp448(b), p, false); p = __builtin_amdgcn_cvt_pk_fp8_f32(clamp448(c), clamp448(d), p, true); return (unsigned)p; }
; __device__ __forceinline__ void conv8b_run(const Ctx& X, int first, int step, int count) {
;     ...
;         for (int q = 0; q < 4; ++q) { u32x4 o;
;             o.x = pk_fp8x4(v[0][q] * W8_SCALE, v[1][q] * W8_SCALE, v[2][q] * W8_SCALE, v[3][q] * W8_SCALE); o.y = pk_fp8x4(v[4][q] * W8_SCALE, v[5][q] * W8_SCALE, v[6][q] * W8_SCALE, v[7][q] * W8_SCALE);
;             o.z = pk_fp8x4(v[8][q] * W8_SCALE, v[9][q] * W8_SCALE, v[10][q] * W8_SCALE, v[11][q] * W8_SCALE); o.w = pk_fp8x4(v[12][q] * W8_SCALE, v[13][q] * W8_SCALE, v[14][q] * W8_SCALE, v[15][q] * W8_SCALE);
;             *(LAS u32x4*)(buf + (4 * X.lane + q) * CVT_STRIDE + 16 * X.wave) = o; }
	v_cvt_pk_fp8_f32 v82, v85, v83
	v_mul_f32_e32 v84, 0x42800000, v11
	v_mul_f32_e32 v83, 0x42800000, v43
	v_med3_f32 v84, v84, s14, v78
	v_med3_f32 v83, v83, s14, v78
	v_cvt_pk_fp8_f32 v82, v84, v83 op_sel:[0,0,1]
	v_mul_f32_e32 v83, 0x42800000, v7
	v_mul_f32_e32 v84, 0x42800000, v39
	v_med3_f32 v86, v83, s14, v78
	v_med3_f32 v84, v84, s14, v78

; #define LAS __attribute__((address_space(3)))
; __device__ __forceinline__ float clamp448(float x) { return fminf(fmaxf(x, -448.f), 448.f); }
; __device__ __forceinline__ unsigned pk_fp8x4(float a, float b, float c, float d) {
;     int p = 0; p = __builtin_amdgcn_cvt_pk_fp8_f32(clamp448(a), clamp448(b), p, false); p = __builtin_amdgcn_cvt_pk_fp8_f32(clamp448(c), clamp448(d), p, true); return (unsigned)p; }
; __device__ __forceinline__ void conv8b_run(const Ctx& X, int first, int step, int count) {
;     ...
;         for (int q = 0; q < 4; ++q) { u32x4 o;
;             o.x = pk_fp8x4(v[0][q] * W8_SCALE, v[1][q] * W8_SCALE, v[2][q] * W8_SCALE, v[3][q] * W8_SCALE); o.y = pk_fp8x4(v[4][q] * W8_SCALE, v[5][q] * W8_SCALE, v[6][q] * W8_SCALE, v[7][q] * W8_SCALE);
;             o.z = pk_fp8x4(v[8][q] * W8_SCALE, v[9][q] * W8_SCALE, v[10][q] * W8_SCALE, v[11][q] * W8_SCALE); o.w = pk_fp8x4(v[12][q] * W8_SCALE, v[13][q] * W8_SCALE, v[14][q] * W8_SCALE, v[15][q] * W8_SCALE);
;             *(LAS u32x4*)(buf + (4 * X.lane + q) * CVT_STRIDE + 16 * X.wave) = o; }
	v_cvt_pk_fp8_f32 v83, v86, v84
	v_mul_f32_e32 v85, 0x42800000, v3
	v_mul_f32_e32 v84, 0x42800000, v35
	v_med3_f32 v85, v85, s14, v78
	v_med3_f32 v84, v84, s14, v78
	v_cvt_pk_fp8_f32 v83, v85, v84 op_sel:[0,0,1]
	v_mul_f32_e32 v84, 0x42800000, v64
	v_mul_f32_e32 v85, 0x42800000, v32
	v_med3_f32 v87, v84, s14, v78
	v_med3_f32 v85, v85, s14, v78

; #define LAS __attribute__((address_space(3)))
; __device__ __forceinline__ float clamp448(float x) { return fminf(fmaxf(x, -448.f), 448.f); }
; __device__ __forceinline__ unsigned pk_fp8x4(float a, float b, float c, float d) {
;     int p = 0; p = __builtin_amdgcn_cvt_pk_fp8_f32(clamp448(a), clamp448(b), p, false); p = __builtin_amdgcn_cvt_pk_fp8_f32(clamp448(c), clamp448(d), p, true); return (unsigned)p; }
; __device__ __forceinline__ void conv8b_run(const Ctx& X, int first, int step, int count) {
;     ...
;         for (int q = 0; q < 4; ++q) { u32x4 o;
;             o.x = pk_fp8x4(v[0][q] * W8_SCALE, v[1][q] * W8_SCALE, v[2][q] * W8_SCALE, v[3][q] * W8_SCALE); o.y = pk_fp8x4(v[4][q] * W8_SCALE, v[5][q] * W8_SCALE, v[6][q] * W8_SCALE, v[7][q] * W8_SCALE);
;             o.z = pk_fp8x4(v[8][q] * W8_SCALE, v[9][q] * W8_SCALE, v[10][q] * W8_SCALE, v[11][q] * W8_SCALE); o.w = pk_fp8x4(v[12][q] * W8_SCALE, v[13][q] * W8_SCALE, v[14][q] * W8_SCALE, v[15][q] * W8_SCALE);
;             *(LAS u32x4*)(buf + (4 * X.lane + q) * CVT_STRIDE + 16 * X.wave) = o; }
	v_cvt_pk_fp8_f32 v84, v87, v85
	v_mul_f32_e32 v86, 0x42800000, v28
	v_mul_f32_e32 v85, 0x42800000, v60
	v_med3_f32 v86, v86, s14, v78
	v_med3_f32 v85, v85, s14, v78
	v_cvt_pk_fp8_f32 v84, v86, v85 op_sel:[0,0,1]
	v_mul_f32_e32 v85, 0x42800000, v24
	v_mul_f32_e32 v86, 0x42800000, v56
	v_med3_f32 v88, v85, s14, v78
	v_med3_f32 v86, v86, s14, v78

; #define LAS __attribute__((address_space(3)))
; __device__ __forceinline__ float clamp448(float x) { return fminf(fmaxf(x, -448.f), 448.f); }
; __device__ __forceinline__ unsigned pk_fp8x4(float a, float b, float c, float d) {
;     int p = 0; p = __builtin_amdgcn_cvt_pk_fp8_f32(clamp448(a), clamp448(b), p, false); p = __builtin_amdgcn_cvt_pk_fp8_f32(clamp448(c), clamp448(d), p, true); return (unsigned)p; }
; __device__ __forceinline__ void conv8b_run(const Ctx& X, int first, int step, int count) {
;     ...
;         for (int q = 0; q < 4; ++q) { u32x4 o;
;             o.x = pk_fp8x4(v[0][q] * W8_SCALE, v[1][q] * W8_SCALE, v[2][q] * W8_SCALE, v[3][q] * W8_SCALE); o.y = pk_fp8x4(v[4][q] * W8_SCALE, v[5][q] * W8_SCALE, v[6][q] * W8_SCALE, v[7][q] * W8_SCALE);
;             o.z = pk_fp8x4(v[8][q] * W8_SCALE, v[9][q] * W8_SCALE, v[10][q] * W8_SCALE, v[11][q] * W8_SCALE); o.w = pk_fp8x4(v[12][q] * W8_SCALE, v[13][q] * W8_SCALE, v[14][q] * W8_SCALE, v[15][q] * W8_SCALE);
;             *(LAS u32x4*)(buf + (4 * X.lane + q) * CVT_STRIDE + 16 * X.wave) = o; }
	v_cvt_pk_fp8_f32 v85, v88, v86
	v_mul_f32_e32 v87, 0x42800000, v20
	v_mul_f32_e32 v86, 0x42800000, v52
	v_med3_f32 v87, v87, s14, v78
	v_med3_f32 v86, v86, s14, v78
	v_cvt_pk_fp8_f32 v85, v87, v86 op_sel:[0,0,1]
	v_mul_f32_e32 v86, 0x42800000, v16
	v_mul_f32_e32 v87, 0x42800000, v48
	v_med3_f32 v89, v86, s14, v78
	v_med3_f32 v87, v87, s14, v78

; #define LAS __attribute__((address_space(3)))
; __device__ __forceinline__ float clamp448(float x) { return fminf(fmaxf(x, -448.f), 448.f); }
; __device__ __forceinline__ unsigned pk_fp8x4(float a, float b, float c, float d) {
;     int p = 0; p = __builtin_amdgcn_cvt_pk_fp8_f32(clamp448(a), clamp448(b), p, false); p = __builtin_amdgcn_cvt_pk_fp8_f32(clamp448(c), clamp448(d), p, true); return (unsigned)p; }
; __device__ __forceinline__ void conv8b_run(const Ctx& X, int first, int step, int count) {
;     ...
;         for (int q = 0; q < 4; ++q) { u32x4 o;
;             o.x = pk_fp8x4(v[0][q] * W8_SCALE, v[1][q] * W8_SCALE, v[2][q] * W8_SCALE, v[3][q] * W8_SCALE); o.y = pk_fp8x4(v[4][q] * W8_SCALE, v[5][q] * W8_SCALE, v[6][q] * W8_SCALE, v[7][q] * W8_SCALE);
;             o.z = pk_fp8x4(v[8][q] * W8_SCALE, v[9][q] * W8_SCALE, v[10][q] * W8_SCALE, v[11][q] * W8_SCALE); o.w = pk_fp8x4(v[12][q] * W8_SCALE, v[13][q] * W8_SCALE, v[14][q] * W8_SCALE, v[15][q] * W8_SCALE);
;             *(LAS u32x4*)(buf + (4 * X.lane + q) * CVT_STRIDE + 16 * X.wave) = o; }
	v_cvt_pk_fp8_f32 v86, v89, v87
	v_mul_f32_e32 v88, 0x42800000, v12
	v_mul_f32_e32 v87, 0x42800000, v44
	v_med3_f32 v88, v88, s14, v78
	v_med3_f32 v87, v87, s14, v78
	v_cvt_pk_fp8_f32 v86, v88, v87 op_sel:[0,0,1]
	v_mul_f32_e32 v87, 0x42800000, v8
	v_mul_f32_e32 v88, 0x42800000, v40
	v_med3_f32 v90, v87, s14, v78
	v_med3_f32 v88, v88, s14, v78

; #define LAS __attribute__((address_space(3)))
; __device__ __forceinline__ float clamp448(float x) { return fminf(fmaxf(x, -448.f), 448.f); }
; __device__ __forceinline__ unsigned pk_fp8x4(float a, float b, float c, float d) {
;     int p = 0; p = __builtin_amdgcn_cvt_pk_fp8_f32(clamp448(a), clamp448(b), p, false); p = __builtin_amdgcn_cvt_pk_fp8_f32(clamp448(c), clamp448(d), p, true); return (unsigned)p; }
; __device__ __forceinline__ void conv8b_run(const Ctx& X, int first, int step, int count) {
;     ...
;         for (int q = 0; q < 4; ++q) { u32x4 o;
;             o.x = pk_fp8x4(v[0][q] * W8_SCALE, v[1][q] * W8_SCALE, v[2][q] * W8_SCALE, v[3][q] * W8_SCALE); o.y = pk_fp8x4(v[4][q] * W8_SCALE, v[5][q] * W8_SCALE, v[6][q] * W8_SCALE, v[7][q] * W8_SCALE);
;             o.z = pk_fp8x4(v[8][q] * W8_SCALE, v[9][q] * W8_SCALE, v[10][q] * W8_SCALE, v[11][q] * W8_SCALE); o.w = pk_fp8x4(v[12][q] * W8_SCALE, v[13][q] * W8_SCALE, v[14][q] * W8_SCALE, v[15][q] * W8_SCALE);
;             *(LAS u32x4*)(buf + (4 * X.lane + q) * CVT_STRIDE + 16 * X.wave) = o; }
	v_cvt_pk_fp8_f32 v87, v90, v88
	v_mul_f32_e32 v89, 0x42800000, v4
	v_mul_f32_e32 v88, 0x42800000, v36
	v_med3_f32 v89, v89, s14, v78
	v_med3_f32 v88, v88, s14, v78
	v_cvt_pk_fp8_f32 v87, v89, v88 op_sel:[0,0,1]
	v_mul_f32_e32 v88, 0x42800000, v65
	v_mul_f32_e32 v89, 0x42800000, v33
	v_med3_f32 v91, v88, s14, v78
	v_med3_f32 v89, v89, s14, v78

; #define LAS __attribute__((address_space(3)))
; __device__ __forceinline__ float clamp448(float x) { return fminf(fmaxf(x, -448.f), 448.f); }
; __device__ __forceinline__ unsigned pk_fp8x4(float a, float b, float c, float d) {
;     int p = 0; p = __builtin_amdgcn_cvt_pk_fp8_f32(clamp448(a), clamp448(b), p, false); p = __builtin_amdgcn_cvt_pk_fp8_f32(clamp448(c), clamp448(d), p, true); return (unsigned)p; }
; __device__ __forceinline__ void conv8b_run(const Ctx& X, int first, int step, int count) {
;     ...
;         for (int q = 0; q < 4; ++q) { u32x4 o;
;             o.x = pk_fp8x4(v[0][q] * W8_SCALE, v[1][q] * W8_SCALE, v[2][q] * W8_SCALE, v[3][q] * W8_SCALE); o.y = pk_fp8x4(v[4][q] * W8_SCALE, v[5][q] * W8_SCALE, v[6][q] * W8_SCALE, v[7][q] * W8_SCALE);
;             o.z = pk_fp8x4(v[8][q] * W8_SCALE, v[9][q] * W8_SCALE, v[10][q] * W8_SCALE, v[11][q] * W8_SCALE); o.w = pk_fp8x4(v[12][q] * W8_SCALE, v[13][q] * W8_SCALE, v[14][q] * W8_SCALE, v[15][q] * W8_SCALE);
;             *(LAS u32x4*)(buf + (4 * X.lane + q) * CVT_STRIDE + 16 * X.wave) = o; }
	v_cvt_pk_fp8_f32 v88, v91, v89
	v_mul_f32_e32 v90, 0x42800000, v29
	v_mul_f32_e32 v89, 0x42800000, v61
	v_med3_f32 v90, v90, s14, v78
	v_med3_f32 v89, v89, s14, v78
	v_cvt_pk_fp8_f32 v88, v90, v89 op_sel:[0,0,1]
	v_mul_f32_e32 v89, 0x42800000, v25
	v_mul_f32_e32 v90, 0x42800000, v57
	v_med3_f32 v92, v89, s14, v78
	v_med3_f32 v90, v90, s14, v78

; #define LAS __attribute__((address_space(3)))
; __device__ __forceinline__ float clamp448(float x) { return fminf(fmaxf(x, -448.f), 448.f); }
; __device__ __forceinline__ unsigned pk_fp8x4(float a, float b, float c, float d) {
;     int p = 0; p = __builtin_amdgcn_cvt_pk_fp8_f32(clamp448(a), clamp448(b), p, false); p = __builtin_amdgcn_cvt_pk_fp8_f32(clamp448(c), clamp448(d), p, true); return (unsigned)p; }
; __device__ __forceinline__ void conv8b_run(const Ctx& X, int first, int step, int count) {
;     ...
;         for (int q = 0; q < 4; ++q) { u32x4 o;
;             o.x = pk_fp8x4(v[0][q] * W8_SCALE, v[1][q] * W8_SCALE, v[2][q] * W8_SCALE, v[3][q] * W8_SCALE); o.y = pk_fp8x4(v[4][q] * W8_SCALE, v[5][q] * W8_SCALE, v[6][q] * W8_SCALE, v[7][q] * W8_SCALE);
;             o.z = pk_fp8x4(v[8][q] * W8_SCALE, v[9][q] * W8_SCALE, v[10][q] * W8_SCALE, v[11][q] * W8_SCALE); o.w = pk_fp8x4(v[12][q] * W8_SCALE, v[13][q] * W8_SCALE, v[14][q] * W8_SCALE, v[15][q] * W8_SCALE);
;             *(LAS u32x4*)(buf + (4 * X.lane + q) * CVT_STRIDE + 16 * X.wave) = o; }
	v_cvt_pk_fp8_f32 v89, v92, v90
	v_mul_f32_e32 v91, 0x42800000, v21
	v_mul_f32_e32 v90, 0x42800000, v53
	v_med3_f32 v91, v91, s14, v78
	v_med3_f32 v90, v90, s14, v78
	v_cvt_pk_fp8_f32 v89, v91, v90 op_sel:[0,0,1]
	v_mul_f32_e32 v90, 0x42800000, v17
	v_mul_f32_e32 v91, 0x42800000, v49
	v_med3_f32 v93, v90, s14, v78
	v_med3_f32 v91, v91, s14, v78

; #define LAS __attribute__((address_space(3)))
; __device__ __forceinline__ float clamp448(float x) { return fminf(fmaxf(x, -448.f), 448.f); }
; __device__ __forceinline__ unsigned pk_fp8x4(float a, float b, float c, float d) {
;     int p = 0; p = __builtin_amdgcn_cvt_pk_fp8_f32(clamp448(a), clamp448(b), p, false); p = __builtin_amdgcn_cvt_pk_fp8_f32(clamp448(c), clamp448(d), p, true); return (unsigned)p; }
; __device__ __forceinline__ void conv8b_run(const Ctx& X, int first, int step, int count) {
;     ...
;         for (int q = 0; q < 4; ++q) { u32x4 o;
;             o.x = pk_fp8x4(v[0][q] * W8_SCALE, v[1][q] * W8_SCALE, v[2][q] * W8_SCALE, v[3][q] * W8_SCALE); o.y = pk_fp8x4(v[4][q] * W8_SCALE, v[5][q] * W8_SCALE, v[6][q] * W8_SCALE, v[7][q] * W8_SCALE);
;             o.z = pk_fp8x4(v[8][q] * W8_SCALE, v[9][q] * W8_SCALE, v[10][q] * W8_SCALE, v[11][q] * W8_SCALE); o.w = pk_fp8x4(v[12][q] * W8_SCALE, v[13][q] * W8_SCALE, v[14][q] * W8_SCALE, v[15][q] * W8_SCALE);
;             *(LAS u32x4*)(buf + (4 * X.lane + q) * CVT_STRIDE + 16 * X.wave) = o; }
	v_cvt_pk_fp8_f32 v90, v93, v91
	v_mul_f32_e32 v92, 0x42800000, v13
	v_mul_f32_e32 v91, 0x42800000, v45
	v_med3_f32 v92, v92, s14, v78
	v_med3_f32 v91, v91, s14, v78
	v_cvt_pk_fp8_f32 v90, v92, v91 op_sel:[0,0,1]
	v_mul_f32_e32 v91, 0x42800000, v9
	v_mul_f32_e32 v92, 0x42800000, v41
	v_med3_f32 v94, v91, s14, v78
	v_med3_f32 v92, v92, s14, v78

; #define LAS __attribute__((address_space(3)))
; __device__ __forceinline__ Cvb conv8b_dec(const Ctx& X, int bit) { Cvb c; int kb, nb;
;     if (bit < I_GU8 / 8) { const int e = bit >> 8, r = bit & 255; kb = r >> 4; nb = r & 15; c.N = 2 * DFF; c.W = XP_w_gu(X) + (size_t)e * D * (2 * DFF); c.WT = XP_WguT(X) + (size_t)e * 16 * PAN_GU + (size_t)kb * PAN_GU; }
;     else { const int b2 = bit - I_GU8 / 8, e = b2 >> 7, r = b2 & 127; kb = r >> 3; nb = r & 7; c.N = D; c.W = XP_w_d(X) + (size_t)e * DFF * D; c.WT = XP_WdT(X) + (size_t)e * 16 * PAN_D + (size_t)kb * PAN_D; }
;     c.W += (size_t)(kb * 128 + 16 * X.wave) * c.N + nb * 256 + 4 * X.lane;
;     c.WT += (size_t)(nb * 256 + 32 * X.wave + (X.lane >> 3)) * 128 + 16 * (X.lane & 7);
;     return c; }
; __device__ __forceinline__ void conv8b_run(const Ctx& X, int first, int step, int count) {
;     ...
;         for (int q = 0; q < 4; ++q) { u32x4 o;
;             o.x = pk_fp8x4(v[0][q] * W8_SCALE, v[1][q] * W8_SCALE, v[2][q] * W8_SCALE, v[3][q] * W8_SCALE); o.y = pk_fp8x4(v[4][q] * W8_SCALE, v[5][q] * W8_SCALE, v[6][q] * W8_SCALE, v[7][q] * W8_SCALE);
;             o.z = pk_fp8x4(v[8][q] * W8_SCALE, v[9][q] * W8_SCALE, v[10][q] * W8_SCALE, v[11][q] * W8_SCALE); o.w = pk_fp8x4(v[12][q] * W8_SCALE, v[13][q] * W8_SCALE, v[14][q] * W8_SCALE, v[15][q] * W8_SCALE);
;             *(LAS u32x4*)(buf + (4 * X.lane + q) * CVT_STRIDE + 16 * X.wave) = o; }
;         if (j + 1 < count) { cn = conv8b_dec(X, first + (j + 1) * step);
; #pragma unroll
;             for (int i = 0; i < 16; ++i) v[i] = __builtin_nontemporal_load((const f32x4*)(cn.W + (size_t)i * cn.N)); }
	v_cvt_pk_fp8_f32 v91, v94, v92
	v_mul_f32_e32 v93, 0x42800000, v5
	v_mul_f32_e32 v92, 0x42800000, v37
	v_med3_f32 v93, v93, s14, v78
	v_med3_f32 v92, v92, s14, v78
	v_cvt_pk_fp8_f32 v91, v93, v92 op_sel:[0,0,1]
	s_cmp_gt_u32 s16, 1
	ds_write_b128 v79, v[80:83] offset:144
	ds_write_b128 v79, v[84:87] offset:288
	ds_write_b128 v79, v[88:91] offset:432
	s_cbranch_scc1 .LBB0_476
	s_add_i32 s2, s13, 0xffffe000
	s_mov_b64 s[6:7], s[100:101]
	s_bfe_u32 s18, s13, 0x40003
	s_lshr_b32 s2, s2, 7
	s_lshl_b32 s19, s18, 18
	s_lshl_b64 s[8:9], s[2:3], 22
	s_add_u32 s20, s10, s8
	s_addc_u32 s21, s11, s9
	s_lshl_b64 s[8:9], s[2:3], 24
	s_waitcnt lgkmcnt(0)
	s_add_u32 s22, s6, s8
	s_addc_u32 s23, s7, s9
	s_add_u32 s6, s20, s19
	s_addc_u32 s7, s21, 0
	s_lshl_b32 s2, s18, 7
	s_add_i32 s2, s2, s12
	s_lshl_b64 s[8:9], s[2:3], 13
	s_add_u32 s2, s22, s8
	s_addc_u32 s9, s23, s9
	s_add_u32 s8, s2, s15
	s_addc_u32 s9, s9, 0
	v_lshl_add_u64 v[34:35], s[8:9], 0, v[66:67]
	v_add_co_u32_e32 v2, vcc, 0x2000, v34
	s_nop 1
	v_addc_co_u32_e32 v3, vcc, 0, v35, vcc
	v_add_co_u32_e32 v4, vcc, 0x4000, v34
	s_nop 1
	v_addc_co_u32_e32 v5, vcc, 0, v35, vcc
	global_load_dwordx4 v[30:33], v[2:3], off nt
	global_load_dwordx4 v[26:29], v[4:5], off nt
	v_add_co_u32_e32 v2, vcc, 0x6000, v34
	s_nop 1
	v_addc_co_u32_e32 v3, vcc, 0, v35, vcc
	v_add_co_u32_e32 v4, vcc, 0x8000, v34
	s_nop 1
	v_addc_co_u32_e32 v5, vcc, 0, v35, vcc
	global_load_dwordx4 v[58:61], v[2:3], off nt
	global_load_dwordx4 v[22:25], v[4:5], off nt
	v_add_co_u32_e32 v2, vcc, 0xa000, v34
	s_nop 1
	v_addc_co_u32_e32 v3, vcc, 0, v35, vcc
	v_add_co_u32_e32 v4, vcc, 0xc000, v34
	s_nop 1
	v_addc_co_u32_e32 v5, vcc, 0, v35, vcc
	global_load_dwordx4 v[54:57], v[2:3], off nt
	global_load_dwordx4 v[18:21], v[4:5], off nt
	v_add_co_u32_e32 v2, vcc, 0xe000, v34
	s_nop 1
	v_addc_co_u32_e32 v3, vcc, 0, v35, vcc
	v_add_co_u32_e32 v4, vcc, 0x10000, v34
	s_nop 1
	v_addc_co_u32_e32 v5, vcc, 0, v35, vcc
	global_load_dwordx4 v[50:53], v[2:3], off nt
	global_load_dwordx4 v[14:17], v[4:5], off nt
	v_add_co_u32_e32 v2, vcc, 0x12000, v34
	s_nop 1
	v_addc_co_u32_e32 v3, vcc, 0, v35, vcc
	v_add_co_u32_e32 v4, vcc, 0x14000, v34
	s_nop 1
	v_addc_co_u32_e32 v5, vcc, 0, v35, vcc
	global_load_dwordx4 v[46:49], v[2:3], off nt
	global_load_dwordx4 v[10:13], v[4:5], off nt
	v_add_co_u32_e32 v2, vcc, 0x16000, v34
	s_nop 1
	v_addc_co_u32_e32 v3, vcc, 0, v35, vcc
	v_add_co_u32_e32 v4, vcc, 0x18000, v34
	s_nop 1
	v_addc_co_u32_e32 v5, vcc, 0, v35, vcc
	v_add_co_u32_e32 v36, vcc, 0x1a000, v34
	global_load_dwordx4 v[42:45], v[2:3], off nt
	global_load_dwordx4 v[6:9], v[4:5], off nt
	v_addc_co_u32_e32 v37, vcc, 0, v35, vcc
	v_add_co_u32_e32 v62, vcc, 0x1c000, v34
	s_nop 1
	v_addc_co_u32_e32 v63, vcc, 0, v35, vcc
	v_add_co_u32_e32 v74, vcc, 0x1e000, v34
	global_load_dwordx4 v[38:41], v[36:37], off nt
	global_load_dwordx4 v[2:5], v[62:63], off nt
	v_addc_co_u32_e32 v75, vcc, 0, v35, vcc
	global_load_dwordx4 v[62:65], v66, s[8:9] nt
	global_load_dwordx4 v[34:37], v[74:75], off nt
	v_lshl_add_u64 v[74:75], s[6:7], 0, v[70:71]
	v_lshl_add_u64 v[74:75], v[74:75], 0, v[68:69]
	s_branch .LBB0_476

; #define LAS __attribute__((address_space(3)))
; __device__ __forceinline__ float clamp448(float x) { return fminf(fmaxf(x, -448.f), 448.f); }
; __device__ __forceinline__ unsigned pk_fp8x4(float a, float b, float c, float d) {
;     int p = 0; p = __builtin_amdgcn_cvt_pk_fp8_f32(clamp448(a), clamp448(b), p, false); p = __builtin_amdgcn_cvt_pk_fp8_f32(clamp448(c), clamp448(d), p, true); return (unsigned)p; }
; __device__ __forceinline__ void conv8b_run(const Ctx& X, int first, int step, int count) {
;     ...
;         for (int q = 0; q < 4; ++q) { u32x4 o;
;             o.x = pk_fp8x4(v[0][q] * W8_SCALE, v[1][q] * W8_SCALE, v[2][q] * W8_SCALE, v[3][q] * W8_SCALE); o.y = pk_fp8x4(v[4][q] * W8_SCALE, v[5][q] * W8_SCALE, v[6][q] * W8_SCALE, v[7][q] * W8_SCALE);
;             o.z = pk_fp8x4(v[8][q] * W8_SCALE, v[9][q] * W8_SCALE, v[10][q] * W8_SCALE, v[11][q] * W8_SCALE); o.w = pk_fp8x4(v[12][q] * W8_SCALE, v[13][q] * W8_SCALE, v[14][q] * W8_SCALE, v[15][q] * W8_SCALE);
;             *(LAS u32x4*)(buf + (4 * X.lane + q) * CVT_STRIDE + 16 * X.wave) = o; }
.LBB0_665:
	s_waitcnt vmcnt(4)
	v_mul_f32_e32 v78, 0x42800000, v54
	v_mul_f32_e32 v79, 0x42800000, v62
	v_med3_f32 v81, v78, s26, v77
	v_med3_f32 v79, v79, s26, v77

; #define LAS __attribute__((address_space(3)))
; __device__ __forceinline__ float clamp448(float x) { return fminf(fmaxf(x, -448.f), 448.f); }
; __device__ __forceinline__ unsigned pk_fp8x4(float a, float b, float c, float d) {
;     int p = 0; p = __builtin_amdgcn_cvt_pk_fp8_f32(clamp448(a), clamp448(b), p, false); p = __builtin_amdgcn_cvt_pk_fp8_f32(clamp448(c), clamp448(d), p, true); return (unsigned)p; }
; __device__ __forceinline__ void conv8b_run(const Ctx& X, int first, int step, int count) {
;     ...
;         for (int q = 0; q < 4; ++q) { u32x4 o;
;             o.x = pk_fp8x4(v[0][q] * W8_SCALE, v[1][q] * W8_SCALE, v[2][q] * W8_SCALE, v[3][q] * W8_SCALE); o.y = pk_fp8x4(v[4][q] * W8_SCALE, v[5][q] * W8_SCALE, v[6][q] * W8_SCALE, v[7][q] * W8_SCALE);
;             o.z = pk_fp8x4(v[8][q] * W8_SCALE, v[9][q] * W8_SCALE, v[10][q] * W8_SCALE, v[11][q] * W8_SCALE); o.w = pk_fp8x4(v[12][q] * W8_SCALE, v[13][q] * W8_SCALE, v[14][q] * W8_SCALE, v[15][q] * W8_SCALE);
;             *(LAS u32x4*)(buf + (4 * X.lane + q) * CVT_STRIDE + 16 * X.wave) = o; }
	v_cvt_pk_fp8_f32 v78, v81, v79
	v_mul_f32_e32 v80, 0x42800000, v50
	v_mul_f32_e32 v79, 0x42800000, v58
	v_med3_f32 v80, v80, s26, v77
	v_med3_f32 v79, v79, s26, v77
	v_cvt_pk_fp8_f32 v78, v80, v79 op_sel:[0,0,1]
	v_mul_f32_e32 v79, 0x42800000, v42
	v_mul_f32_e32 v80, 0x42800000, v46
	v_med3_f32 v82, v79, s26, v77
	v_med3_f32 v80, v80, s26, v77

; #define LAS __attribute__((address_space(3)))
; __device__ __forceinline__ float clamp448(float x) { return fminf(fmaxf(x, -448.f), 448.f); }
; __device__ __forceinline__ unsigned pk_fp8x4(float a, float b, float c, float d) {
;     int p = 0; p = __builtin_amdgcn_cvt_pk_fp8_f32(clamp448(a), clamp448(b), p, false); p = __builtin_amdgcn_cvt_pk_fp8_f32(clamp448(c), clamp448(d), p, true); return (unsigned)p; }
; __device__ __forceinline__ void conv8b_run(const Ctx& X, int first, int step, int count) {
;     ...
;         for (int q = 0; q < 4; ++q) { u32x4 o;
;             o.x = pk_fp8x4(v[0][q] * W8_SCALE, v[1][q] * W8_SCALE, v[2][q] * W8_SCALE, v[3][q] * W8_SCALE); o.y = pk_fp8x4(v[4][q] * W8_SCALE, v[5][q] * W8_SCALE, v[6][q] * W8_SCALE, v[7][q] * W8_SCALE);
;             o.z = pk_fp8x4(v[8][q] * W8_SCALE, v[9][q] * W8_SCALE, v[10][q] * W8_SCALE, v[11][q] * W8_SCALE); o.w = pk_fp8x4(v[12][q] * W8_SCALE, v[13][q] * W8_SCALE, v[14][q] * W8_SCALE, v[15][q] * W8_SCALE);
;             *(LAS u32x4*)(buf + (4 * X.lane + q) * CVT_STRIDE + 16 * X.wave) = o; }
	v_cvt_pk_fp8_f32 v79, v82, v80
	v_mul_f32_e32 v81, 0x42800000, v34
	v_mul_f32_e32 v80, 0x42800000, v38
	v_med3_f32 v81, v81, s26, v77
	v_med3_f32 v80, v80, s26, v77
	v_cvt_pk_fp8_f32 v79, v81, v80 op_sel:[0,0,1]
	v_mul_f32_e32 v80, 0x42800000, v30
	v_mul_f32_e32 v81, 0x42800000, v26
	v_med3_f32 v83, v80, s26, v77
	v_med3_f32 v81, v81, s26, v77

; #define LAS __attribute__((address_space(3)))
; __device__ __forceinline__ float clamp448(float x) { return fminf(fmaxf(x, -448.f), 448.f); }
; __device__ __forceinline__ unsigned pk_fp8x4(float a, float b, float c, float d) {
;     int p = 0; p = __builtin_amdgcn_cvt_pk_fp8_f32(clamp448(a), clamp448(b), p, false); p = __builtin_amdgcn_cvt_pk_fp8_f32(clamp448(c), clamp448(d), p, true); return (unsigned)p; }
; __device__ __forceinline__ void conv8b_run(const Ctx& X, int first, int step, int count) {
;     ...
;         for (int q = 0; q < 4; ++q) { u32x4 o;
;             o.x = pk_fp8x4(v[0][q] * W8_SCALE, v[1][q] * W8_SCALE, v[2][q] * W8_SCALE, v[3][q] * W8_SCALE); o.y = pk_fp8x4(v[4][q] * W8_SCALE, v[5][q] * W8_SCALE, v[6][q] * W8_SCALE, v[7][q] * W8_SCALE);
;             o.z = pk_fp8x4(v[8][q] * W8_SCALE, v[9][q] * W8_SCALE, v[10][q] * W8_SCALE, v[11][q] * W8_SCALE); o.w = pk_fp8x4(v[12][q] * W8_SCALE, v[13][q] * W8_SCALE, v[14][q] * W8_SCALE, v[15][q] * W8_SCALE);
;             *(LAS u32x4*)(buf + (4 * X.lane + q) * CVT_STRIDE + 16 * X.wave) = o; }
	v_cvt_pk_fp8_f32 v80, v83, v81
	v_mul_f32_e32 v82, 0x42800000, v22
	v_mul_f32_e32 v81, 0x42800000, v18
	v_med3_f32 v82, v82, s26, v77
	v_med3_f32 v81, v81, s26, v77
	v_cvt_pk_fp8_f32 v80, v82, v81 op_sel:[0,0,1]
	v_mul_f32_e32 v81, 0x42800000, v14
	v_mul_f32_e32 v82, 0x42800000, v10
	v_med3_f32 v84, v81, s26, v77
	v_med3_f32 v82, v82, s26, v77

; #define LAS __attribute__((address_space(3)))
; __device__ __forceinline__ float clamp448(float x) { return fminf(fmaxf(x, -448.f), 448.f); }
; __device__ __forceinline__ unsigned pk_fp8x4(float a, float b, float c, float d) {
;     int p = 0; p = __builtin_amdgcn_cvt_pk_fp8_f32(clamp448(a), clamp448(b), p, false); p = __builtin_amdgcn_cvt_pk_fp8_f32(clamp448(c), clamp448(d), p, true); return (unsigned)p; }
; __device__ __forceinline__ void conv8b_run(const Ctx& X, int first, int step, int count) {
;     ...
;         for (int q = 0; q < 4; ++q) { u32x4 o;
;             o.x = pk_fp8x4(v[0][q] * W8_SCALE, v[1][q] * W8_SCALE, v[2][q] * W8_SCALE, v[3][q] * W8_SCALE); o.y = pk_fp8x4(v[4][q] * W8_SCALE, v[5][q] * W8_SCALE, v[6][q] * W8_SCALE, v[7][q] * W8_SCALE);
;             o.z = pk_fp8x4(v[8][q] * W8_SCALE, v[9][q] * W8_SCALE, v[10][q] * W8_SCALE, v[11][q] * W8_SCALE); o.w = pk_fp8x4(v[12][q] * W8_SCALE, v[13][q] * W8_SCALE, v[14][q] * W8_SCALE, v[15][q] * W8_SCALE);
;             *(LAS u32x4*)(buf + (4 * X.lane + q) * CVT_STRIDE + 16 * X.wave) = o; }
	v_cvt_pk_fp8_f32 v81, v84, v82
	v_mul_f32_e32 v83, 0x42800000, v6
	v_mul_f32_e32 v82, 0x42800000, v2
	s_bitcmp1_b32 s27, 0
	v_med3_f32 v83, v83, s26, v77
	v_med3_f32 v82, v82, s26, v77
	s_cselect_b32 s2, 0x9000, 0
	v_cvt_pk_fp8_f32 v81, v83, v82 op_sel:[0,0,1]
	s_add_i32 s28, s2, 0
	s_add_i32 s2, s20, s28
	v_add_u32_e32 v90, s2, v74
	ds_write_b128 v90, v[78:81]
	v_mul_f32_e32 v78, 0x42800000, v55
	v_mul_f32_e32 v79, 0x42800000, v63
	v_med3_f32 v81, v78, s26, v77
	v_med3_f32 v79, v79, s26, v77

; #define LAS __attribute__((address_space(3)))
; __device__ __forceinline__ float clamp448(float x) { return fminf(fmaxf(x, -448.f), 448.f); }
; __device__ __forceinline__ unsigned pk_fp8x4(float a, float b, float c, float d) {
;     int p = 0; p = __builtin_amdgcn_cvt_pk_fp8_f32(clamp448(a), clamp448(b), p, false); p = __builtin_amdgcn_cvt_pk_fp8_f32(clamp448(c), clamp448(d), p, true); return (unsigned)p; }
; __device__ __forceinline__ void conv8b_run(const Ctx& X, int first, int step, int count) {
;     ...
;         for (int q = 0; q < 4; ++q) { u32x4 o;
;             o.x = pk_fp8x4(v[0][q] * W8_SCALE, v[1][q] * W8_SCALE, v[2][q] * W8_SCALE, v[3][q] * W8_SCALE); o.y = pk_fp8x4(v[4][q] * W8_SCALE, v[5][q] * W8_SCALE, v[6][q] * W8_SCALE, v[7][q] * W8_SCALE);
;             o.z = pk_fp8x4(v[8][q] * W8_SCALE, v[9][q] * W8_SCALE, v[10][q] * W8_SCALE, v[11][q] * W8_SCALE); o.w = pk_fp8x4(v[12][q] * W8_SCALE, v[13][q] * W8_SCALE, v[14][q] * W8_SCALE, v[15][q] * W8_SCALE);
;             *(LAS u32x4*)(buf + (4 * X.lane + q) * CVT_STRIDE + 16 * X.wave) = o; }
	v_cvt_pk_fp8_f32 v78, v81, v79
	v_mul_f32_e32 v80, 0x42800000, v51
	v_mul_f32_e32 v79, 0x42800000, v59
	v_med3_f32 v80, v80, s26, v77
	v_med3_f32 v79, v79, s26, v77
	v_cvt_pk_fp8_f32 v78, v80, v79 op_sel:[0,0,1]
	v_mul_f32_e32 v79, 0x42800000, v43
	v_mul_f32_e32 v80, 0x42800000, v47
	v_med3_f32 v82, v79, s26, v77
	v_med3_f32 v80, v80, s26, v77

; #define LAS __attribute__((address_space(3)))
; __device__ __forceinline__ float clamp448(float x) { return fminf(fmaxf(x, -448.f), 448.f); }
; __device__ __forceinline__ unsigned pk_fp8x4(float a, float b, float c, float d) {
;     int p = 0; p = __builtin_amdgcn_cvt_pk_fp8_f32(clamp448(a), clamp448(b), p, false); p = __builtin_amdgcn_cvt_pk_fp8_f32(clamp448(c), clamp448(d), p, true); return (unsigned)p; }
; __device__ __forceinline__ void conv8b_run(const Ctx& X, int first, int step, int count) {
;     ...
;         for (int q = 0; q < 4; ++q) { u32x4 o;
;             o.x = pk_fp8x4(v[0][q] * W8_SCALE, v[1][q] * W8_SCALE, v[2][q] * W8_SCALE, v[3][q] * W8_SCALE); o.y = pk_fp8x4(v[4][q] * W8_SCALE, v[5][q] * W8_SCALE, v[6][q] * W8_SCALE, v[7][q] * W8_SCALE);
;             o.z = pk_fp8x4(v[8][q] * W8_SCALE, v[9][q] * W8_SCALE, v[10][q] * W8_SCALE, v[11][q] * W8_SCALE); o.w = pk_fp8x4(v[12][q] * W8_SCALE, v[13][q] * W8_SCALE, v[14][q] * W8_SCALE, v[15][q] * W8_SCALE);
;             *(LAS u32x4*)(buf + (4 * X.lane + q) * CVT_STRIDE + 16 * X.wave) = o; }
	v_cvt_pk_fp8_f32 v79, v82, v80
	v_mul_f32_e32 v81, 0x42800000, v35
	v_mul_f32_e32 v80, 0x42800000, v39
	v_med3_f32 v81, v81, s26, v77
	v_med3_f32 v80, v80, s26, v77
	v_cvt_pk_fp8_f32 v79, v81, v80 op_sel:[0,0,1]
	v_mul_f32_e32 v80, 0x42800000, v31
	v_mul_f32_e32 v81, 0x42800000, v27
	v_med3_f32 v83, v80, s26, v77
	v_med3_f32 v81, v81, s26, v77

; #define LAS __attribute__((address_space(3)))
; __device__ __forceinline__ float clamp448(float x) { return fminf(fmaxf(x, -448.f), 448.f); }
; __device__ __forceinline__ unsigned pk_fp8x4(float a, float b, float c, float d) {
;     int p = 0; p = __builtin_amdgcn_cvt_pk_fp8_f32(clamp448(a), clamp448(b), p, false); p = __builtin_amdgcn_cvt_pk_fp8_f32(clamp448(c), clamp448(d), p, true); return (unsigned)p; }
; __device__ __forceinline__ void conv8b_run(const Ctx& X, int first, int step, int count) {
;     ...
;         for (int q = 0; q < 4; ++q) { u32x4 o;
;             o.x = pk_fp8x4(v[0][q] * W8_SCALE, v[1][q] * W8_SCALE, v[2][q] * W8_SCALE, v[3][q] * W8_SCALE); o.y = pk_fp8x4(v[4][q] * W8_SCALE, v[5][q] * W8_SCALE, v[6][q] * W8_SCALE, v[7][q] * W8_SCALE);
;             o.z = pk_fp8x4(v[8][q] * W8_SCALE, v[9][q] * W8_SCALE, v[10][q] * W8_SCALE, v[11][q] * W8_SCALE); o.w = pk_fp8x4(v[12][q] * W8_SCALE, v[13][q] * W8_SCALE, v[14][q] * W8_SCALE, v[15][q] * W8_SCALE);
;             *(LAS u32x4*)(buf + (4 * X.lane + q) * CVT_STRIDE + 16 * X.wave) = o; }
	v_cvt_pk_fp8_f32 v80, v83, v81
	v_mul_f32_e32 v82, 0x42800000, v23
	v_mul_f32_e32 v81, 0x42800000, v19
	v_med3_f32 v82, v82, s26, v77
	v_med3_f32 v81, v81, s26, v77
	v_cvt_pk_fp8_f32 v80, v82, v81 op_sel:[0,0,1]
	v_mul_f32_e32 v81, 0x42800000, v15
	v_mul_f32_e32 v82, 0x42800000, v11
	v_med3_f32 v84, v81, s26, v77
	v_med3_f32 v82, v82, s26, v77

; #define LAS __attribute__((address_space(3)))
; __device__ __forceinline__ float clamp448(float x) { return fminf(fmaxf(x, -448.f), 448.f); }
; __device__ __forceinline__ unsigned pk_fp8x4(float a, float b, float c, float d) {
;     int p = 0; p = __builtin_amdgcn_cvt_pk_fp8_f32(clamp448(a), clamp448(b), p, false); p = __builtin_amdgcn_cvt_pk_fp8_f32(clamp448(c), clamp448(d), p, true); return (unsigned)p; }
; __device__ __forceinline__ void conv8b_run(const Ctx& X, int first, int step, int count) {
;     ...
;         for (int q = 0; q < 4; ++q) { u32x4 o;
;             o.x = pk_fp8x4(v[0][q] * W8_SCALE, v[1][q] * W8_SCALE, v[2][q] * W8_SCALE, v[3][q] * W8_SCALE); o.y = pk_fp8x4(v[4][q] * W8_SCALE, v[5][q] * W8_SCALE, v[6][q] * W8_SCALE, v[7][q] * W8_SCALE);
;             o.z = pk_fp8x4(v[8][q] * W8_SCALE, v[9][q] * W8_SCALE, v[10][q] * W8_SCALE, v[11][q] * W8_SCALE); o.w = pk_fp8x4(v[12][q] * W8_SCALE, v[13][q] * W8_SCALE, v[14][q] * W8_SCALE, v[15][q] * W8_SCALE);
;             *(LAS u32x4*)(buf + (4 * X.lane + q) * CVT_STRIDE + 16 * X.wave) = o; }
	v_cvt_pk_fp8_f32 v81, v84, v82
	v_mul_f32_e32 v83, 0x42800000, v7
	v_mul_f32_e32 v82, 0x42800000, v3
	v_med3_f32 v83, v83, s26, v77
	v_med3_f32 v82, v82, s26, v77
	v_cvt_pk_fp8_f32 v81, v83, v82 op_sel:[0,0,1]
	v_mul_f32_e32 v82, 0x42800000, v56
	v_mul_f32_e32 v83, 0x42800000, v64
	v_med3_f32 v85, v82, s26, v77
	v_med3_f32 v83, v83, s26, v77

; #define LAS __attribute__((address_space(3)))
; __device__ __forceinline__ float clamp448(float x) { return fminf(fmaxf(x, -448.f), 448.f); }
; __device__ __forceinline__ unsigned pk_fp8x4(float a, float b, float c, float d) {
;     int p = 0; p = __builtin_amdgcn_cvt_pk_fp8_f32(clamp448(a), clamp448(b), p, false); p = __builtin_amdgcn_cvt_pk_fp8_f32(clamp448(c), clamp448(d), p, true); return (unsigned)p; }
; __device__ __forceinline__ void conv8b_run(const Ctx& X, int first, int step, int count) {
;     ...
;         for (int q = 0; q < 4; ++q) { u32x4 o;
;             o.x = pk_fp8x4(v[0][q] * W8_SCALE, v[1][q] * W8_SCALE, v[2][q] * W8_SCALE, v[3][q] * W8_SCALE); o.y = pk_fp8x4(v[4][q] * W8_SCALE, v[5][q] * W8_SCALE, v[6][q] * W8_SCALE, v[7][q] * W8_SCALE);
;             o.z = pk_fp8x4(v[8][q] * W8_SCALE, v[9][q] * W8_SCALE, v[10][q] * W8_SCALE, v[11][q] * W8_SCALE); o.w = pk_fp8x4(v[12][q] * W8_SCALE, v[13][q] * W8_SCALE, v[14][q] * W8_SCALE, v[15][q] * W8_SCALE);
;             *(LAS u32x4*)(buf + (4 * X.lane + q) * CVT_STRIDE + 16 * X.wave) = o; }
	v_cvt_pk_fp8_f32 v82, v85, v83
	v_mul_f32_e32 v84, 0x42800000, v52
	v_mul_f32_e32 v83, 0x42800000, v60
	v_med3_f32 v84, v84, s26, v77
	v_med3_f32 v83, v83, s26, v77
	v_cvt_pk_fp8_f32 v82, v84, v83 op_sel:[0,0,1]
	v_mul_f32_e32 v83, 0x42800000, v44
	v_mul_f32_e32 v84, 0x42800000, v48
	v_med3_f32 v86, v83, s26, v77
	v_med3_f32 v84, v84, s26, v77

; #define LAS __attribute__((address_space(3)))
; __device__ __forceinline__ float clamp448(float x) { return fminf(fmaxf(x, -448.f), 448.f); }
; __device__ __forceinline__ unsigned pk_fp8x4(float a, float b, float c, float d) {
;     int p = 0; p = __builtin_amdgcn_cvt_pk_fp8_f32(clamp448(a), clamp448(b), p, false); p = __builtin_amdgcn_cvt_pk_fp8_f32(clamp448(c), clamp448(d), p, true); return (unsigned)p; }
; __device__ __forceinline__ void conv8b_run(const Ctx& X, int first, int step, int count) {
;     ...
;         for (int q = 0; q < 4; ++q) { u32x4 o;
;             o.x = pk_fp8x4(v[0][q] * W8_SCALE, v[1][q] * W8_SCALE, v[2][q] * W8_SCALE, v[3][q] * W8_SCALE); o.y = pk_fp8x4(v[4][q] * W8_SCALE, v[5][q] * W8_SCALE, v[6][q] * W8_SCALE, v[7][q] * W8_SCALE);
;             o.z = pk_fp8x4(v[8][q] * W8_SCALE, v[9][q] * W8_SCALE, v[10][q] * W8_SCALE, v[11][q] * W8_SCALE); o.w = pk_fp8x4(v[12][q] * W8_SCALE, v[13][q] * W8_SCALE, v[14][q] * W8_SCALE, v[15][q] * W8_SCALE);
;             *(LAS u32x4*)(buf + (4 * X.lane + q) * CVT_STRIDE + 16 * X.wave) = o; }
	v_cvt_pk_fp8_f32 v83, v86, v84
	v_mul_f32_e32 v85, 0x42800000, v36
	v_mul_f32_e32 v84, 0x42800000, v40
	v_med3_f32 v85, v85, s26, v77
	v_med3_f32 v84, v84, s26, v77
	v_cvt_pk_fp8_f32 v83, v85, v84 op_sel:[0,0,1]
	v_mul_f32_e32 v84, 0x42800000, v32
	v_mul_f32_e32 v85, 0x42800000, v28
	v_med3_f32 v87, v84, s26, v77
	v_med3_f32 v85, v85, s26, v77

; #define LAS __attribute__((address_space(3)))
; __device__ __forceinline__ float clamp448(float x) { return fminf(fmaxf(x, -448.f), 448.f); }
; __device__ __forceinline__ unsigned pk_fp8x4(float a, float b, float c, float d) {
;     int p = 0; p = __builtin_amdgcn_cvt_pk_fp8_f32(clamp448(a), clamp448(b), p, false); p = __builtin_amdgcn_cvt_pk_fp8_f32(clamp448(c), clamp448(d), p, true); return (unsigned)p; }
; __device__ __forceinline__ void conv8b_run(const Ctx& X, int first, int step, int count) {
;     ...
;         for (int q = 0; q < 4; ++q) { u32x4 o;
;             o.x = pk_fp8x4(v[0][q] * W8_SCALE, v[1][q] * W8_SCALE, v[2][q] * W8_SCALE, v[3][q] * W8_SCALE); o.y = pk_fp8x4(v[4][q] * W8_SCALE, v[5][q] * W8_SCALE, v[6][q] * W8_SCALE, v[7][q] * W8_SCALE);
;             o.z = pk_fp8x4(v[8][q] * W8_SCALE, v[9][q] * W8_SCALE, v[10][q] * W8_SCALE, v[11][q] * W8_SCALE); o.w = pk_fp8x4(v[12][q] * W8_SCALE, v[13][q] * W8_SCALE, v[14][q] * W8_SCALE, v[15][q] * W8_SCALE);
;             *(LAS u32x4*)(buf + (4 * X.lane + q) * CVT_STRIDE + 16 * X.wave) = o; }
	v_cvt_pk_fp8_f32 v84, v87, v85
	v_mul_f32_e32 v86, 0x42800000, v24
	v_mul_f32_e32 v85, 0x42800000, v20
	v_med3_f32 v86, v86, s26, v77
	v_med3_f32 v85, v85, s26, v77
	v_cvt_pk_fp8_f32 v84, v86, v85 op_sel:[0,0,1]
	v_mul_f32_e32 v85, 0x42800000, v16
	v_mul_f32_e32 v86, 0x42800000, v12
	v_med3_f32 v88, v85, s26, v77
	v_med3_f32 v86, v86, s26, v77

; #define LAS __attribute__((address_space(3)))
; __device__ __forceinline__ float clamp448(float x) { return fminf(fmaxf(x, -448.f), 448.f); }
; __device__ __forceinline__ unsigned pk_fp8x4(float a, float b, float c, float d) {
;     int p = 0; p = __builtin_amdgcn_cvt_pk_fp8_f32(clamp448(a), clamp448(b), p, false); p = __builtin_amdgcn_cvt_pk_fp8_f32(clamp448(c), clamp448(d), p, true); return (unsigned)p; }
; __device__ __forceinline__ void conv8b_run(const Ctx& X, int first, int step, int count) {
;     ...
;         for (int q = 0; q < 4; ++q) { u32x4 o;
;             o.x = pk_fp8x4(v[0][q] * W8_SCALE, v[1][q] * W8_SCALE, v[2][q] * W8_SCALE, v[3][q] * W8_SCALE); o.y = pk_fp8x4(v[4][q] * W8_SCALE, v[5][q] * W8_SCALE, v[6][q] * W8_SCALE, v[7][q] * W8_SCALE);
;             o.z = pk_fp8x4(v[8][q] * W8_SCALE, v[9][q] * W8_SCALE, v[10][q] * W8_SCALE, v[11][q] * W8_SCALE); o.w = pk_fp8x4(v[12][q] * W8_SCALE, v[13][q] * W8_SCALE, v[14][q] * W8_SCALE, v[15][q] * W8_SCALE);
;             *(LAS u32x4*)(buf + (4 * X.lane + q) * CVT_STRIDE + 16 * X.wave) = o; }
	v_cvt_pk_fp8_f32 v85, v88, v86
	v_mul_f32_e32 v87, 0x42800000, v8
	v_mul_f32_e32 v86, 0x42800000, v4
	v_med3_f32 v87, v87, s26, v77
	v_med3_f32 v86, v86, s26, v77
	v_cvt_pk_fp8_f32 v85, v87, v86 op_sel:[0,0,1]
	v_mul_f32_e32 v86, 0x42800000, v57
	v_mul_f32_e32 v87, 0x42800000, v65
	v_med3_f32 v89, v86, s26, v77
	v_med3_f32 v87, v87, s26, v77

; __device__ __forceinline__ float clamp448(float x) { return fminf(fmaxf(x, -448.f), 448.f); }
; __device__ __forceinline__ unsigned pk_fp8x4(float a, float b, float c, float d) {
;     int p = 0; p = __builtin_amdgcn_cvt_pk_fp8_f32(clamp448(a), clamp448(b), p, false); p = __builtin_amdgcn_cvt_pk_fp8_f32(clamp448(c), clamp448(d), p, true); return (unsigned)p; }
; __device__ __forceinline__ void conv8b_run(const Ctx& X, int first, int step, int count) {
;     ...
;         for (int q = 0; q < 4; ++q) { u32x4 o;
;             o.x = pk_fp8x4(v[0][q] * W8_SCALE, v[1][q] * W8_SCALE, v[2][q] * W8_SCALE, v[3][q] * W8_SCALE); o.y = pk_fp8x4(v[4][q] * W8_SCALE, v[5][q] * W8_SCALE, v[6][q] * W8_SCALE, v[7][q] * W8_SCALE);
;             o.z = pk_fp8x4(v[8][q] * W8_SCALE, v[9][q] * W8_SCALE, v[10][q] * W8_SCALE, v[11][q] * W8_SCALE); o.w = pk_fp8x4(v[12][q] * W8_SCALE, v[13][q] * W8_SCALE, v[14][q] * W8_SCALE, v[15][q] * W8_SCALE);
	v_cvt_pk_fp8_f32 v86, v89, v87
	v_mul_f32_e32 v88, 0x42800000, v53
	v_mul_f32_e32 v87, 0x42800000, v61
	v_med3_f32 v88, v88, s26, v77
	v_med3_f32 v87, v87, s26, v77
	v_cvt_pk_fp8_f32 v86, v88, v87 op_sel:[0,0,1]
	v_mul_f32_e32 v87, 0x42800000, v45
	v_mul_f32_e32 v88, 0x42800000, v49
	v_med3_f32 v91, v87, s26, v77
	v_med3_f32 v88, v88, s26, v77

; __device__ __forceinline__ float clamp448(float x) { return fminf(fmaxf(x, -448.f), 448.f); }
; __device__ __forceinline__ unsigned pk_fp8x4(float a, float b, float c, float d) {
;     int p = 0; p = __builtin_amdgcn_cvt_pk_fp8_f32(clamp448(a), clamp448(b), p, false); p = __builtin_amdgcn_cvt_pk_fp8_f32(clamp448(c), clamp448(d), p, true); return (unsigned)p; }
; __device__ __forceinline__ void conv8b_run(const Ctx& X, int first, int step, int count) {
;     ...
;         for (int q = 0; q < 4; ++q) { u32x4 o;
;             o.x = pk_fp8x4(v[0][q] * W8_SCALE, v[1][q] * W8_SCALE, v[2][q] * W8_SCALE, v[3][q] * W8_SCALE); o.y = pk_fp8x4(v[4][q] * W8_SCALE, v[5][q] * W8_SCALE, v[6][q] * W8_SCALE, v[7][q] * W8_SCALE);
;             o.z = pk_fp8x4(v[8][q] * W8_SCALE, v[9][q] * W8_SCALE, v[10][q] * W8_SCALE, v[11][q] * W8_SCALE); o.w = pk_fp8x4(v[12][q] * W8_SCALE, v[13][q] * W8_SCALE, v[14][q] * W8_SCALE, v[15][q] * W8_SCALE);
	v_cvt_pk_fp8_f32 v87, v91, v88
	v_mul_f32_e32 v89, 0x42800000, v37
	v_mul_f32_e32 v88, 0x42800000, v41
	v_med3_f32 v89, v89, s26, v77
	v_med3_f32 v88, v88, s26, v77
	v_cvt_pk_fp8_f32 v87, v89, v88 op_sel:[0,0,1]
	v_mul_f32_e32 v88, 0x42800000, v33
	v_mul_f32_e32 v89, 0x42800000, v29
	v_med3_f32 v92, v88, s26, v77
	v_med3_f32 v89, v89, s26, v77

; __device__ __forceinline__ float clamp448(float x) { return fminf(fmaxf(x, -448.f), 448.f); }
; __device__ __forceinline__ unsigned pk_fp8x4(float a, float b, float c, float d) {
;     int p = 0; p = __builtin_amdgcn_cvt_pk_fp8_f32(clamp448(a), clamp448(b), p, false); p = __builtin_amdgcn_cvt_pk_fp8_f32(clamp448(c), clamp448(d), p, true); return (unsigned)p; }
; __device__ __forceinline__ void conv8b_run(const Ctx& X, int first, int step, int count) {
;     ...
;         for (int q = 0; q < 4; ++q) { u32x4 o;
;             o.x = pk_fp8x4(v[0][q] * W8_SCALE, v[1][q] * W8_SCALE, v[2][q] * W8_SCALE, v[3][q] * W8_SCALE); o.y = pk_fp8x4(v[4][q] * W8_SCALE, v[5][q] * W8_SCALE, v[6][q] * W8_SCALE, v[7][q] * W8_SCALE);
;             o.z = pk_fp8x4(v[8][q] * W8_SCALE, v[9][q] * W8_SCALE, v[10][q] * W8_SCALE, v[11][q] * W8_SCALE); o.w = pk_fp8x4(v[12][q] * W8_SCALE, v[13][q] * W8_SCALE, v[14][q] * W8_SCALE, v[15][q] * W8_SCALE);
	v_cvt_pk_fp8_f32 v88, v92, v89
	v_mul_f32_e32 v91, 0x42800000, v25
	v_mul_f32_e32 v89, 0x42800000, v21
	v_med3_f32 v91, v91, s26, v77
	v_med3_f32 v89, v89, s26, v77
	v_cvt_pk_fp8_f32 v88, v91, v89 op_sel:[0,0,1]
	v_mul_f32_e32 v89, 0x42800000, v17
	v_mul_f32_e32 v91, 0x42800000, v13
	v_med3_f32 v93, v89, s26, v77
	v_med3_f32 v91, v91, s26, v77

; #define LAS __attribute__((address_space(3)))
; __device__ __forceinline__ void conv8b_run(const Ctx& X, int first, int step, int count) {
;     ...
;         for (int q = 0; q < 4; ++q) { u32x4 o;
;             o.x = pk_fp8x4(v[0][q] * W8_SCALE, v[1][q] * W8_SCALE, v[2][q] * W8_SCALE, v[3][q] * W8_SCALE); o.y = pk_fp8x4(v[4][q] * W8_SCALE, v[5][q] * W8_SCALE, v[6][q] * W8_SCALE, v[7][q] * W8_SCALE);
;             o.z = pk_fp8x4(v[8][q] * W8_SCALE, v[9][q] * W8_SCALE, v[10][q] * W8_SCALE, v[11][q] * W8_SCALE); o.w = pk_fp8x4(v[12][q] * W8_SCALE, v[13][q] * W8_SCALE, v[14][q] * W8_SCALE, v[15][q] * W8_SCALE);
;             *(LAS u32x4*)(buf + (4 * X.lane + q) * CVT_STRIDE + 16 * X.wave) = o; }
;         if (j + 1 < count) { cn = conv8b_dec(X, first + (j + 1) * step);
	v_cvt_pk_fp8_f32 v89, v93, v91
	v_mul_f32_e32 v92, 0x42800000, v9
	v_mul_f32_e32 v91, 0x42800000, v5
	v_med3_f32 v92, v92, s26, v77
	v_med3_f32 v91, v91, s26, v77
	v_cvt_pk_fp8_f32 v89, v92, v91 op_sel:[0,0,1]
	s_cmp_gt_u32 s27, 9
	ds_write_b128 v90, v[78:81] offset:144
	ds_write_b128 v90, v[82:85] offset:288
	ds_write_b128 v90, v[86:89] offset:432
	s_cbranch_scc1 .LBB0_664
	s_cmpk_gt_i32 s25, 0x1fff
	s_mov_b64 s[14:15], -1
	s_cbranch_scc0 .LBB0_668
	s_mov_b64 s[8:9], s[100:101]
	s_add_i32 s2, s25, 0xffffe000
	s_lshr_b32 s2, s2, 7
	s_lshl_b64 s[10:11], s[2:3], 24
	s_mov_b64 s[14:15], 0
	s_waitcnt lgkmcnt(0)
	s_add_u32 s8, s8, s10
	s_addc_u32 s9, s9, s11
	s_lshl_b64 s[10:11], s[2:3], 22
	s_add_u32 s10, s18, s10
	s_addc_u32 s11, s19, s11
